# attention: v_max(x,x) canonicalisations feeding max trees and p+0 accumulator inits removed (192+31 instr per loop copy set), wait states re-derived
# speedup vs baseline: 1.0038x; 1.0038x over previous
.LBB0_507:
	ds_read_b128 v[72:75], v191 offset:18432
	ds_read_b128 v[80:83], v191 offset:18496
	s_waitcnt lgkmcnt(1)
	v_mfma_f32_16x16x32_bf16 v[52:55], v[72:75], v[4:7], v[52:55]
	v_mfma_f32_16x16x32_bf16 v[72:75], v[72:75], v[12:15], v[56:59]
	s_waitcnt lgkmcnt(0)
	v_mfma_f32_16x16x32_bf16 v[56:59], v[80:83], v[8:11], v[52:55]
	s_nop 4
	ds_read_b128 v[52:55], v191 offset:20736
	s_waitcnt lgkmcnt(0)
	v_mfma_f32_16x16x32_bf16 v[44:47], v[52:55], v[4:7], v[44:47]
	v_mfma_f32_16x16x32_bf16 v[52:55], v[52:55], v[12:15], v[64:67]
	s_nop 2
	ds_read_b128 v[64:67], v191 offset:20800
	v_mfma_f32_16x16x32_bf16 v[72:75], v[80:83], v[16:19], v[72:75]
	s_waitcnt lgkmcnt(0)
	v_mfma_f32_16x16x32_bf16 v[80:83], v[64:67], v[16:19], v[52:55]
	s_nop 2
	ds_read_b128 v[52:55], v191 offset:23040
	v_mfma_f32_16x16x32_bf16 v[44:47], v[64:67], v[8:11], v[44:47]
	ds_read_b128 v[64:67], v191 offset:23104
	s_waitcnt lgkmcnt(1)
	v_mfma_f32_16x16x32_bf16 v[60:63], v[52:55], v[4:7], v[60:63]
	v_mfma_f32_16x16x32_bf16 v[52:55], v[52:55], v[12:15], v[84:87]
	s_waitcnt lgkmcnt(0)
	v_mfma_f32_16x16x32_bf16 v[84:87], v[64:67], v[16:19], v[52:55]
	v_mfma_f32_16x16x32_bf16 v[148:151], v[64:67], v[8:11], v[60:63]
	s_nop 4
	ds_read_b128 v[52:55], v191 offset:25344
	ds_read_b128 v[60:63], v191 offset:25408
	s_waitcnt lgkmcnt(1)
	v_mfma_f32_16x16x32_bf16 v[48:51], v[52:55], v[4:7], v[48:51]
	v_mfma_f32_16x16x32_bf16 v[52:55], v[52:55], v[12:15], v[100:103]
	s_waitcnt lgkmcnt(0)
	v_mfma_f32_16x16x32_bf16 v[154:157], v[60:63], v[8:11], v[48:51]
	s_nop 4
	v_max_f32_e32 v3, v58, v59
	v_max_f32_e32 v48, v46, v47
	v_max_f32_e32 v49, v148, v149
	v_mfma_f32_16x16x32_bf16 v[100:103], v[60:63], v[16:19], v[52:55]
	v_max_f32_e32 v50, v150, v151
	v_max3_f32 v3, v56, v57, v3
	v_max_f32_e32 v51, v156, v157
	v_max3_f32 v51, v154, v155, v51
	v_max3_f32 v48, v44, v45, v48
	v_max3_f32 v49, v49, v50, v51
	v_max3_f32 v3, v3, v48, v49
	v_mov_b32_e32 v48, v3
	s_nop 1
	v_permlane32_swap_b32_e32 v3, v48
	v_max_f32_e32 v3, v3, v48
	v_mov_b32_e32 v48, v3
	s_nop 1
	v_permlane16_swap_b32_e32 v3, v48
	v_max3_f32 v218, v220, v3, v48
	v_sub_f32_e32 v3, v220, v218
	v_exp_f32_e32 v128, v3
	v_sub_f32_e32 v3, v56, v218
	v_pk_mul_f32 v[52:53], v[104:105], v[128:129] op_sel_hi:[1,0]
	v_exp_f32_e32 v105, v3
	v_sub_f32_e32 v3, v57, v218
	v_pk_mul_f32 v[54:55], v[106:107], v[128:129] op_sel_hi:[1,0]
	v_exp_f32_e32 v107, v3
	v_sub_f32_e32 v3, v58, v218
	v_pk_mul_f32 v[48:49], v[112:113], v[128:129] op_sel_hi:[1,0]
	v_exp_f32_e32 v113, v3
	v_sub_f32_e32 v3, v59, v218
	v_pk_mul_f32 v[50:51], v[114:115], v[128:129] op_sel_hi:[1,0]
	v_exp_f32_e32 v115, v3
	v_sub_f32_e32 v3, v44, v218
	v_exp_f32_e32 v133, v3
	v_sub_f32_e32 v3, v45, v218
	v_exp_f32_e32 v137, v3
	v_sub_f32_e32 v3, v46, v218
	v_exp_f32_e32 v139, v3
	v_sub_f32_e32 v3, v47, v218
	v_exp_f32_e32 v147, v3
	v_sub_f32_e32 v3, v148, v218
	v_exp_f32_e32 v135, v3
	v_sub_f32_e32 v3, v149, v218
	v_exp_f32_e32 v141, v3
	v_sub_f32_e32 v3, v150, v218
	v_exp_f32_e32 v143, v3
	v_sub_f32_e32 v3, v151, v218
	v_exp_f32_e32 v149, v3
	v_sub_f32_e32 v3, v154, v218
	v_exp_f32_e32 v151, v3
	v_sub_f32_e32 v3, v155, v218
	v_exp_f32_e32 v153, v3
	v_sub_f32_e32 v3, v156, v218
	v_exp_f32_e32 v155, v3
	v_sub_f32_e32 v3, v157, v218
	v_pk_mul_f32 v[64:65], v[92:93], v[128:129] op_sel_hi:[1,0]
	v_exp_f32_e32 v157, v3
	v_max_f32_e32 v3, v74, v75
	v_pk_mul_f32 v[66:67], v[94:95], v[128:129] op_sel_hi:[1,0]
	v_max_f32_e32 v92, v82, v83
	v_max_f32_e32 v93, v84, v85
	v_pk_mul_f32 v[60:61], v[96:97], v[128:129] op_sel_hi:[1,0]
	v_max_f32_e32 v94, v86, v87
	v_max_f32_e32 v95, v102, v103
	v_max3_f32 v95, v100, v101, v95
	v_max3_f32 v3, v72, v73, v3
	v_max3_f32 v92, v80, v81, v92
	v_max3_f32 v93, v93, v94, v95
	v_max3_f32 v3, v3, v92, v93
	v_mov_b32_e32 v92, v3
	s_nop 1
	v_permlane32_swap_b32_e32 v3, v92
	v_max_f32_e32 v3, v3, v92
	v_mov_b32_e32 v92, v3
	s_nop 1
	v_permlane16_swap_b32_e32 v3, v92
	v_max3_f32 v217, v219, v3, v92
	v_sub_f32_e32 v3, v219, v217
	v_exp_f32_e32 v220, v3
	v_sub_f32_e32 v3, v72, v217
	v_exp_f32_e32 v104, v3
	v_sub_f32_e32 v3, v73, v217
	v_exp_f32_e32 v106, v3
	v_sub_f32_e32 v3, v74, v217
	v_exp_f32_e32 v112, v3
	v_sub_f32_e32 v3, v75, v217
	v_exp_f32_e32 v114, v3
	v_sub_f32_e32 v3, v80, v217
	v_exp_f32_e32 v132, v3
	v_sub_f32_e32 v3, v81, v217
	v_exp_f32_e32 v136, v3
	v_sub_f32_e32 v3, v82, v217
	v_exp_f32_e32 v138, v3
	v_sub_f32_e32 v3, v83, v217
	v_exp_f32_e32 v146, v3
	v_sub_f32_e32 v3, v84, v217
	v_exp_f32_e32 v134, v3
	v_sub_f32_e32 v3, v85, v217
	v_exp_f32_e32 v140, v3
	v_sub_f32_e32 v3, v86, v217
	v_exp_f32_e32 v142, v3
	v_sub_f32_e32 v3, v87, v217
	v_exp_f32_e32 v148, v3
	v_sub_f32_e32 v3, v100, v217
	v_exp_f32_e32 v150, v3
	v_sub_f32_e32 v3, v101, v217
	v_exp_f32_e32 v152, v3
	v_sub_f32_e32 v3, v102, v217
	v_exp_f32_e32 v154, v3
	v_sub_f32_e32 v3, v103, v217
	v_exp_f32_e32 v156, v3
	v_pk_mul_f32 v[94:95], v[78:79], v[220:221] op_sel_hi:[1,0]
	v_pk_mul_f32 v[92:93], v[76:77], v[220:221] op_sel_hi:[1,0]
	v_pk_add_f32 v[72:73], v[132:133], v[104:105]
	v_pk_add_f32 v[74:75], v[136:137], v[106:107]
	v_pk_add_f32 v[76:77], v[138:139], v[112:113]
	v_pk_add_f32 v[78:79], v[146:147], v[114:115]
	v_pk_add_f32 v[72:73], v[134:135], v[72:73]
	v_pk_add_f32 v[74:75], v[140:141], v[74:75]
	v_pk_add_f32 v[76:77], v[142:143], v[76:77]
	v_pk_add_f32 v[78:79], v[148:149], v[78:79]
	v_pk_add_f32 v[72:73], v[150:151], v[72:73]
	v_pk_add_f32 v[74:75], v[152:153], v[74:75]
	v_pk_add_f32 v[76:77], v[154:155], v[76:77]
	v_pk_add_f32 v[78:79], v[156:157], v[78:79]
	v_pk_add_f32 v[72:73], v[72:73], v[74:75]
	v_pk_add_f32 v[74:75], v[76:77], v[78:79]
	v_pk_mul_f32 v[62:63], v[98:99], v[128:129] op_sel_hi:[1,0]
	v_pk_mul_f32 v[98:99], v[70:71], v[220:221] op_sel_hi:[1,0]
	v_pk_mul_f32 v[96:97], v[68:69], v[220:221] op_sel_hi:[1,0]
	v_pk_mul_f32 v[90:91], v[90:91], v[220:221] op_sel_hi:[1,0]
	v_pk_mul_f32 v[88:89], v[88:89], v[220:221] op_sel_hi:[1,0]
	v_pk_mul_f32 v[70:71], v[110:111], v[220:221] op_sel_hi:[1,0]
	v_pk_mul_f32 v[68:69], v[108:109], v[220:221] op_sel_hi:[1,0]
	v_mov_b32_e32 v221, v128
	v_pk_add_f32 v[72:73], v[72:73], v[74:75]
	v_cvt_pk_bf16_f32 v56, v105, v107
	v_cvt_pk_bf16_f32 v57, v113, v115
	v_cvt_pk_bf16_f32 v58, v133, v137
	v_cvt_pk_bf16_f32 v59, v139, v147
	v_cvt_pk_bf16_f32 v44, v135, v141
	v_cvt_pk_bf16_f32 v45, v143, v149
	v_cvt_pk_bf16_f32 v46, v151, v153
	v_cvt_pk_bf16_f32 v47, v155, v157
	s_nop 0
	v_pk_fma_f32 v[128:129], v[130:131], v[220:221], v[72:73]
	v_cvt_pk_bf16_f32 v72, v104, v106
	v_cvt_pk_bf16_f32 v73, v112, v114
	v_cvt_pk_bf16_f32 v74, v132, v136
	v_cvt_pk_bf16_f32 v75, v138, v146
	v_cvt_pk_bf16_f32 v76, v134, v140
	v_cvt_pk_bf16_f32 v77, v142, v148
	v_cvt_pk_bf16_f32 v78, v150, v152
	v_cvt_pk_bf16_f32 v79, v154, v156
	ds_read_b64_tr_b16 v[82:83], v192 offset:29952
	ds_read_b64_tr_b16 v[80:81], v192 offset:27648
	ds_read_b64_tr_b16 v[84:85], v192 offset:27680
	ds_read_b64_tr_b16 v[86:87], v192 offset:29984
	s_waitcnt lgkmcnt(0)
	v_mfma_f32_16x16x32_bf16 v[60:63], v[84:87], v[56:59], v[60:63]
	v_mfma_f32_16x16x32_bf16 v[84:87], v[84:87], v[72:75], v[92:95]
	s_nop 2
	ds_read_b64_tr_b16 v[92:93], v192 offset:27712
	ds_read_b64_tr_b16 v[94:95], v192 offset:30016
	v_mfma_f32_16x16x32_bf16 v[64:67], v[80:83], v[56:59], v[64:67]
	v_mfma_f32_16x16x32_bf16 v[80:83], v[80:83], v[72:75], v[96:99]
	s_waitcnt lgkmcnt(0)
	v_mfma_f32_16x16x32_bf16 v[96:99], v[92:95], v[56:59], v[52:55]
	s_nop 2
	ds_read_b64_tr_b16 v[52:53], v192 offset:27744
	ds_read_b64_tr_b16 v[54:55], v192 offset:30048
	s_waitcnt lgkmcnt(0)
	v_mfma_f32_16x16x32_bf16 v[48:51], v[52:55], v[56:59], v[48:51]
	v_mfma_f32_16x16x32_bf16 v[68:71], v[52:55], v[72:75], v[68:71]
	ds_read_b64_tr_b16 v[54:55], v193 offset:29952
	ds_read_b64_tr_b16 v[52:53], v193 offset:27648
	ds_read_b64_tr_b16 v[56:57], v193 offset:27680
	ds_read_b64_tr_b16 v[58:59], v193 offset:29984
	v_mfma_f32_16x16x32_bf16 v[88:91], v[92:95], v[72:75], v[88:91]
	s_waitcnt lgkmcnt(2)
	v_mfma_f32_16x16x32_bf16 v[72:75], v[52:55], v[44:47], v[64:67]
	v_mfma_f32_16x16x32_bf16 v[52:55], v[52:55], v[76:79], v[80:83]
	s_waitcnt lgkmcnt(0)
	v_mfma_f32_16x16x32_bf16 v[80:83], v[56:59], v[44:47], v[60:63]
	s_nop 2
	ds_read_b64_tr_b16 v[60:61], v193 offset:27712
	ds_read_b64_tr_b16 v[62:63], v193 offset:30016
	ds_read_b64_tr_b16 v[64:65], v193 offset:27744
	ds_read_b64_tr_b16 v[66:67], v193 offset:30048
	v_mfma_f32_16x16x32_bf16 v[56:59], v[56:59], v[76:79], v[84:87]
	s_waitcnt lgkmcnt(2)
	v_mfma_f32_16x16x32_bf16 v[84:87], v[60:63], v[44:47], v[96:99]
	v_mfma_f32_16x16x32_bf16 v[60:63], v[60:63], v[76:79], v[88:91]
	s_waitcnt lgkmcnt(0)
	v_mfma_f32_16x16x32_bf16 v[100:103], v[64:67], v[44:47], v[48:51]
	v_mfma_f32_16x16x32_bf16 v[64:67], v[64:67], v[76:79], v[68:71]

; #define LAS __attribute__((address_space(3)))
; #define ATT_WRITE(buf_, kq_, vq_) do { const int key = F.tid >> 3, ds = (F.tid & 7) * 8; LAS bf16_t* Kd = Ks0 + (buf_) * 9216; LAS bf16_t* Vd = Kd + 4608; \
;             *(LAS u32x4*)(Kd + key * 72 + ds) = kq_; *(LAS u32x4*)(Vd + key * 72 + ds) = vq_; } while (0)
; __device__ __forceinline__ void ph_attn(const Frame& F, int j) {
;     ...
;             const bool loc = ch < nloc; const int kr = rlo + ch;
;             ATT_WRITE((ch + 1) & 1, kw, vw);
;             ATT_LOAD(kl, vl, ch + 4);
;             const LAS bf16_t* Ks = Ks0 + (ch & 1) * 9216; const LAS bf16_t* Vt = Ks + 4608;
;             const bool m0 = (ch < nch) && (loc ? (kr >= r0t[0] && kr < r0t[0] + 8) : true);
;             const bool m1 = (ch < nch) && (loc ? (kr >= r0t[1] && kr < r0t[1] + 8) : true);
;             if (m0 && m1) ATT_COMPUTE(3); else if (m0) ATT_COMPUTE(1); else if (m1) ATT_COMPUTE(2);
.LBB0_509:
	s_add_i32 s0, s30, -3
	v_mov_b32_e32 v44, s13
	v_cmp_lt_i32_e32 vcc, s0, v214
	v_min_i32_e32 v3, s0, v215
	v_mov_b32_e32 v45, s9
	v_cndmask_b32_e32 v44, v216, v44, vcc
	v_mov_b32_e32 v46, s26
	v_add_u32_e32 v3, v44, v3
	v_cndmask_b32_e32 v45, v45, v46, vcc
	v_lshlrev_b32_e32 v3, 6, v3
	v_add_u32_e32 v3, v3, v45
	v_add_u32_e32 v44, v3, v194
	v_ashrrev_i32_e32 v45, 31, v44
	v_lshlrev_b64 v[44:45], 13, v[44:45]
	v_lshl_add_u64 v[48:49], v[0:1], 0, v[44:45]
	global_load_dwordx4 v[44:47], v[48:49], off offset:1024
	s_nop 0
	global_load_dwordx4 v[48:51], v[48:49], off offset:2048
	s_add_i32 s54, s11, s30
	s_add_i32 s0, s30, -7
	s_add_i32 s2, s54, -11
	s_cmp_ge_u32 s2, s24
	v_cmp_ge_i32_e64 s[46:47], s0, v214
	v_cmp_lt_i32_e64 s[48:49], s0, v214
	s_cselect_b64 s[0:1], -1, 0
	s_cmp_lt_u32 s2, s27
	s_cselect_b64 s[4:5], -1, 0
	s_and_b64 s[0:1], s[0:1], s[4:5]
	s_or_b64 s[6:7], s[46:47], s[0:1]
	s_cmp_ge_u32 s2, s25
	s_cselect_b64 s[0:1], -1, 0
	s_cmp_lt_u32 s2, s28
	s_cselect_b64 s[4:5], -1, 0
	s_and_b64 s[0:1], s[0:1], s[4:5]
	s_or_b64 s[4:5], s[46:47], s[0:1]
	s_and_b64 s[0:1], s[6:7], s[4:5]
	s_andn2_b64 vcc, exec, s[0:1]
	s_mov_b64 s[0:1], -1
	s_waitcnt vmcnt(7)
	ds_write_b128 v196, v[28:31] offset:18432
	s_waitcnt vmcnt(6)
	ds_write_b128 v196, v[32:35] offset:27648
	s_cbranch_vccz .LBB0_525
	s_xor_b64 s[6:7], s[6:7], -1
	s_and_b64 vcc, exec, s[6:7]
	s_cbranch_vccz .LBB0_514
	v_mov_b64_e32 v[70:71], v[54:55]
	v_mov_b64_e32 v[78:79], v[58:59]
	v_mov_b64_e32 v[90:91], v[62:63]
	v_mov_b64_e32 v[110:111], v[66:67]
	s_andn2_b64 vcc, exec, s[4:5]
	v_mov_b64_e32 v[130:131], v[128:129]
	v_mov_b32_e32 v134, v217
	v_mov_b64_e32 v[68:69], v[52:53]
	v_mov_b64_e32 v[76:77], v[56:57]
	v_mov_b64_e32 v[88:89], v[60:61]
	v_mov_b64_e32 v[108:109], v[64:65]
	s_cbranch_vccnz .LBB0_513
	v_add_u32_e32 v3, s31, v198
	ds_read_b32 v28, v3 offset:37120
	v_add_u32_e32 v3, s31, v199
	ds_read_b32 v29, v3 offset:37120
	v_add_u32_e32 v3, s31, v200
	ds_read_b32 v30, v3 offset:37120
	v_add_u32_e32 v3, s31, v201
	ds_read_b32 v31, v3 offset:37120
	v_add_u32_e32 v3, s31, v202
	ds_read_b32 v32, v3 offset:37120
	v_add_u32_e32 v3, s31, v203
	ds_read_b32 v33, v3 offset:37120
	v_add_u32_e32 v3, s31, v204
	ds_read_b32 v34, v3 offset:37120
	v_add_u32_e32 v3, s31, v205
	ds_read_b32 v35, v3 offset:37120
	v_add_u32_e32 v3, s31, v206
	ds_read_b32 v68, v3 offset:37120
	v_add_u32_e32 v3, s31, v207
	ds_read_b32 v69, v3 offset:37120
	v_add_u32_e32 v3, s31, v208
	ds_read_b32 v70, v3 offset:37120
	v_add_u32_e32 v3, s31, v209
	ds_read_b32 v71, v3 offset:37120
	v_add_u32_e32 v3, s31, v210
	ds_read_b32 v76, v3 offset:37120
	v_add_u32_e32 v3, s31, v211
	ds_read_b32 v77, v3 offset:37120
	v_add_u32_e32 v3, s31, v212
	ds_read_b32 v78, v3 offset:37120
	v_add_u32_e32 v3, s31, v213
	ds_read_b32 v79, v3 offset:37120
	ds_read_b128 v[88:91], v191
	s_waitcnt lgkmcnt(0)
	v_mfma_f32_16x16x32_bf16 v[28:31], v[88:91], v[12:15], v[28:31]
	ds_read_b128 v[88:91], v191 offset:64
	v_mov_b32_e32 v131, v129
	s_waitcnt lgkmcnt(0)
	v_mfma_f32_16x16x32_bf16 v[28:31], v[88:91], v[16:19], v[28:31]
	ds_read_b128 v[88:91], v191 offset:2304
	s_nop 6
	s_waitcnt lgkmcnt(0)
	v_mfma_f32_16x16x32_bf16 v[32:35], v[88:91], v[12:15], v[32:35]
	ds_read_b128 v[88:91], v191 offset:2368
	s_waitcnt lgkmcnt(0)
	v_mfma_f32_16x16x32_bf16 v[32:35], v[88:91], v[16:19], v[32:35]
	ds_read_b128 v[88:91], v191 offset:4608
	s_waitcnt lgkmcnt(0)
	v_mfma_f32_16x16x32_bf16 v[68:71], v[88:91], v[12:15], v[68:71]
	ds_read_b128 v[88:91], v191 offset:4672
	s_waitcnt lgkmcnt(0)
	v_mfma_f32_16x16x32_bf16 v[68:71], v[88:91], v[16:19], v[68:71]
	ds_read_b128 v[88:91], v191 offset:6912
	s_waitcnt lgkmcnt(0)
	v_mfma_f32_16x16x32_bf16 v[76:79], v[88:91], v[12:15], v[76:79]
	ds_read_b128 v[88:91], v191 offset:6976
	s_waitcnt lgkmcnt(0)
	v_mfma_f32_16x16x32_bf16 v[76:79], v[88:91], v[16:19], v[76:79]
	v_max_f32_e32 v3, v30, v31
	v_max_f32_e32 v88, v34, v35
	v_max_f32_e32 v89, v68, v69
	v_max_f32_e32 v90, v70, v71
	s_nop 3
	v_max_f32_e32 v91, v78, v79
	v_max3_f32 v91, v76, v77, v91
	v_max3_f32 v3, v28, v29, v3
	v_max3_f32 v88, v32, v33, v88
	v_max3_f32 v89, v89, v90, v91
	v_max3_f32 v3, v3, v88, v89
	v_mov_b32_e32 v88, v3
	s_nop 1
	v_permlane32_swap_b32_e32 v3, v88
	v_max_f32_e32 v3, v3, v88
	v_mov_b32_e32 v88, v3
	s_nop 1
	v_permlane16_swap_b32_e32 v3, v88
	v_max3_f32 v134, v217, v3, v88
	v_sub_f32_e32 v3, v217, v134
	v_exp_f32_e32 v108, v3
	v_sub_f32_e32 v3, v28, v134
	v_exp_f32_e32 v28, v3
	v_sub_f32_e32 v3, v29, v134
	v_exp_f32_e32 v110, v3
	v_sub_f32_e32 v3, v30, v134
	v_exp_f32_e32 v29, v3
	v_sub_f32_e32 v3, v31, v134
	v_exp_f32_e32 v111, v3
	v_sub_f32_e32 v3, v32, v134
	v_exp_f32_e32 v30, v3
	v_sub_f32_e32 v3, v33, v134
	v_exp_f32_e32 v32, v3
	v_sub_f32_e32 v3, v34, v134
	v_exp_f32_e32 v31, v3
	v_sub_f32_e32 v3, v35, v134
	v_exp_f32_e32 v33, v3
	v_sub_f32_e32 v3, v68, v134
	v_exp_f32_e32 v34, v3
	v_sub_f32_e32 v3, v69, v134
	v_exp_f32_e32 v68, v3
	v_sub_f32_e32 v3, v70, v134
	v_exp_f32_e32 v35, v3
	v_sub_f32_e32 v3, v71, v134
	v_exp_f32_e32 v69, v3
	v_sub_f32_e32 v3, v76, v134
	v_exp_f32_e32 v70, v3
	v_sub_f32_e32 v3, v77, v134
	v_exp_f32_e32 v76, v3
	v_sub_f32_e32 v3, v78, v134
	v_exp_f32_e32 v71, v3
	v_sub_f32_e32 v3, v79, v134
	v_exp_f32_e32 v77, v3
	v_pk_add_f32 v[78:79], v[30:31], v[28:29]
	v_pk_add_f32 v[112:113], v[32:33], v[110:111]
	v_pk_add_f32 v[78:79], v[34:35], v[78:79]
	v_pk_add_f32 v[112:113], v[68:69], v[112:113]
	v_pk_add_f32 v[78:79], v[70:71], v[78:79]
	v_pk_add_f32 v[112:113], v[76:77], v[112:113]
	v_cvt_pk_bf16_f32 v28, v28, v110
	v_cvt_pk_bf16_f32 v29, v29, v111
	v_cvt_pk_bf16_f32 v30, v30, v32
	v_cvt_pk_bf16_f32 v31, v31, v33
	v_cvt_pk_bf16_f32 v32, v34, v68
	s_nop 0
	v_pk_add_f32 v[78:79], v[78:79], v[112:113]
	v_cvt_pk_bf16_f32 v33, v35, v69
	v_cvt_pk_bf16_f32 v34, v70, v76
	v_cvt_pk_bf16_f32 v35, v71, v77
	ds_read_b64_tr_b16 v[70:71], v192 offset:11520
	ds_read_b64_tr_b16 v[68:69], v192 offset:9216
	ds_read_b64_tr_b16 v[76:77], v192 offset:9248
	v_add_f32_e32 v130, v78, v79
	ds_read_b64_tr_b16 v[78:79], v192 offset:11552
	v_pk_mul_f32 v[90:91], v[54:55], v[108:109] op_sel_hi:[1,0]
	v_pk_mul_f32 v[88:89], v[52:53], v[108:109] op_sel_hi:[1,0]
	v_pk_mul_f32 v[94:95], v[58:59], v[108:109] op_sel_hi:[1,0]
	v_pk_mul_f32 v[92:93], v[56:57], v[108:109] op_sel_hi:[1,0]
	s_waitcnt lgkmcnt(2)
	v_mfma_f32_16x16x32_bf16 v[68:71], v[68:71], v[28:31], v[88:91]
	s_nop 2
	ds_read_b64_tr_b16 v[88:89], v192 offset:9280
	ds_read_b64_tr_b16 v[90:91], v192 offset:11584
	v_pk_mul_f32 v[98:99], v[62:63], v[108:109] op_sel_hi:[1,0]
	v_pk_mul_f32 v[96:97], v[60:61], v[108:109] op_sel_hi:[1,0]
	s_waitcnt lgkmcnt(2)
	v_mfma_f32_16x16x32_bf16 v[76:79], v[76:79], v[28:31], v[92:95]
	s_nop 2
	ds_read_b64_tr_b16 v[92:93], v192 offset:9312
	ds_read_b64_tr_b16 v[94:95], v192 offset:11616
	v_pk_mul_f32 v[106:107], v[66:67], v[108:109] op_sel_hi:[1,0]
	v_pk_mul_f32 v[104:105], v[64:65], v[108:109] op_sel_hi:[1,0]
	s_waitcnt lgkmcnt(2)
	v_mfma_f32_16x16x32_bf16 v[88:91], v[88:91], v[28:31], v[96:99]
	v_fmac_f32_e32 v130, v128, v108
	s_waitcnt lgkmcnt(0)
	v_mfma_f32_16x16x32_bf16 v[28:31], v[92:95], v[28:31], v[104:107]
	ds_read_b64_tr_b16 v[94:95], v193 offset:11520
	ds_read_b64_tr_b16 v[92:93], v193 offset:9216
	ds_read_b64_tr_b16 v[96:97], v193 offset:9248
	ds_read_b64_tr_b16 v[98:99], v193 offset:11552
	s_waitcnt lgkmcnt(2)
	v_mfma_f32_16x16x32_bf16 v[68:71], v[92:95], v[32:35], v[68:71]
	ds_read_b64_tr_b16 v[92:93], v193 offset:9280
	ds_read_b64_tr_b16 v[94:95], v193 offset:11584
	s_waitcnt lgkmcnt(0)
	v_mfma_f32_16x16x32_bf16 v[88:91], v[92:95], v[32:35], v[88:91]
	ds_read_b64_tr_b16 v[92:93], v193 offset:9312
	ds_read_b64_tr_b16 v[94:95], v193 offset:11616
	v_mfma_f32_16x16x32_bf16 v[76:79], v[96:99], v[32:35], v[76:79]
	s_waitcnt lgkmcnt(0)
	v_mfma_f32_16x16x32_bf16 v[108:111], v[92:95], v[32:35], v[28:31]

.LBB0_523:
	ds_read_b128 v[88:91], v191
	v_mov_b32_e32 v130, v128
	v_mov_b32_e32 v134, v217
	s_waitcnt lgkmcnt(0)
	v_mfma_f32_16x16x32_bf16 v[32:35], v[88:91], v[4:7], v[32:35]
	ds_read_b128 v[88:91], v191 offset:64
	s_waitcnt lgkmcnt(0)
	v_mfma_f32_16x16x32_bf16 v[32:35], v[88:91], v[8:11], v[32:35]
	ds_read_b128 v[88:91], v191 offset:2304
	s_nop 6
	s_waitcnt lgkmcnt(0)
	v_mfma_f32_16x16x32_bf16 v[28:31], v[88:91], v[4:7], v[28:31]
	ds_read_b128 v[88:91], v191 offset:2368
	s_waitcnt lgkmcnt(0)
	v_mfma_f32_16x16x32_bf16 v[28:31], v[88:91], v[8:11], v[28:31]
	ds_read_b128 v[88:91], v191 offset:4608
	s_waitcnt lgkmcnt(0)
	v_mfma_f32_16x16x32_bf16 v[76:79], v[88:91], v[4:7], v[76:79]
	ds_read_b128 v[88:91], v191 offset:4672
	s_waitcnt lgkmcnt(0)
	v_mfma_f32_16x16x32_bf16 v[76:79], v[88:91], v[8:11], v[76:79]
	ds_read_b128 v[88:91], v191 offset:6912
	s_waitcnt lgkmcnt(0)
	v_mfma_f32_16x16x32_bf16 v[68:71], v[88:91], v[4:7], v[68:71]
	ds_read_b128 v[88:91], v191 offset:6976
	s_waitcnt lgkmcnt(0)
	v_mfma_f32_16x16x32_bf16 v[68:71], v[88:91], v[8:11], v[68:71]
	v_max_f32_e32 v3, v34, v35
	v_max_f32_e32 v88, v30, v31
	v_max_f32_e32 v89, v76, v77
	v_max_f32_e32 v90, v78, v79
	s_nop 3
	v_max_f32_e32 v91, v70, v71
	v_max3_f32 v91, v68, v69, v91
	v_max3_f32 v3, v32, v33, v3
	v_max3_f32 v88, v28, v29, v88
	v_max3_f32 v89, v89, v90, v91
	v_max3_f32 v3, v3, v88, v89
	v_mov_b32_e32 v88, v3
	s_nop 1
	v_permlane32_swap_b32_e32 v3, v88
	v_max_f32_e32 v3, v3, v88
	v_mov_b32_e32 v88, v3
	s_nop 1
	v_permlane16_swap_b32_e32 v3, v88
	v_max3_f32 v132, v218, v3, v88
	v_sub_f32_e32 v3, v218, v132
	v_exp_f32_e32 v108, v3
	v_sub_f32_e32 v3, v32, v132
	v_exp_f32_e32 v32, v3
	v_sub_f32_e32 v3, v33, v132
	v_exp_f32_e32 v110, v3
	v_sub_f32_e32 v3, v34, v132
	v_exp_f32_e32 v33, v3
	v_sub_f32_e32 v3, v35, v132
	v_exp_f32_e32 v111, v3
	v_sub_f32_e32 v3, v28, v132
	v_exp_f32_e32 v34, v3
	v_sub_f32_e32 v3, v29, v132
	v_exp_f32_e32 v112, v3
	v_sub_f32_e32 v3, v30, v132
	v_exp_f32_e32 v35, v3
	v_sub_f32_e32 v3, v31, v132
	v_exp_f32_e32 v113, v3
	v_sub_f32_e32 v3, v76, v132
	v_exp_f32_e32 v76, v3
	v_sub_f32_e32 v3, v77, v132
	v_exp_f32_e32 v114, v3
	v_sub_f32_e32 v3, v78, v132
	v_exp_f32_e32 v77, v3
	v_sub_f32_e32 v3, v79, v132
	v_exp_f32_e32 v115, v3
	v_sub_f32_e32 v3, v68, v132
	v_exp_f32_e32 v68, v3
	v_sub_f32_e32 v3, v69, v132
	v_exp_f32_e32 v78, v3
	v_sub_f32_e32 v3, v70, v132
	v_exp_f32_e32 v69, v3
	v_sub_f32_e32 v3, v71, v132
	v_exp_f32_e32 v79, v3
	v_pk_add_f32 v[28:29], v[34:35], v[32:33]
	v_pk_add_f32 v[30:31], v[112:113], v[110:111]
	v_pk_add_f32 v[28:29], v[76:77], v[28:29]
	v_pk_add_f32 v[30:31], v[114:115], v[30:31]
	v_pk_add_f32 v[28:29], v[68:69], v[28:29]
	v_pk_add_f32 v[30:31], v[78:79], v[30:31]
	v_pk_mul_f32 v[90:91], v[74:75], v[108:109] op_sel_hi:[1,0]
	v_pk_add_f32 v[28:29], v[28:29], v[30:31]
	v_pk_mul_f32 v[88:89], v[72:73], v[108:109] op_sel_hi:[1,0]
	v_add_f32_e32 v131, v28, v29
	v_cvt_pk_bf16_f32 v28, v32, v110
	v_cvt_pk_bf16_f32 v29, v33, v111
	v_cvt_pk_bf16_f32 v30, v34, v112
	v_cvt_pk_bf16_f32 v31, v35, v113
	v_cvt_pk_bf16_f32 v32, v76, v114
	v_cvt_pk_bf16_f32 v33, v77, v115
	v_cvt_pk_bf16_f32 v34, v68, v78
	v_cvt_pk_bf16_f32 v35, v69, v79
	ds_read_b64_tr_b16 v[70:71], v192 offset:11520
	ds_read_b64_tr_b16 v[68:69], v192 offset:9216
	ds_read_b64_tr_b16 v[76:77], v192 offset:9248
	ds_read_b64_tr_b16 v[78:79], v192 offset:11552
	v_pk_mul_f32 v[94:95], v[82:83], v[108:109] op_sel_hi:[1,0]
	v_pk_mul_f32 v[92:93], v[80:81], v[108:109] op_sel_hi:[1,0]
	s_waitcnt lgkmcnt(2)
	v_mfma_f32_16x16x32_bf16 v[68:71], v[68:71], v[28:31], v[88:91]
	s_nop 2
	ds_read_b64_tr_b16 v[88:89], v192 offset:9280
	ds_read_b64_tr_b16 v[90:91], v192 offset:11584
	v_pk_mul_f32 v[98:99], v[86:87], v[108:109] op_sel_hi:[1,0]
	v_pk_mul_f32 v[96:97], v[84:85], v[108:109] op_sel_hi:[1,0]
	s_waitcnt lgkmcnt(2)
	v_mfma_f32_16x16x32_bf16 v[76:79], v[76:79], v[28:31], v[92:95]
	s_nop 2
	ds_read_b64_tr_b16 v[92:93], v192 offset:9312
	ds_read_b64_tr_b16 v[94:95], v192 offset:11616
	v_pk_mul_f32 v[106:107], v[102:103], v[108:109] op_sel_hi:[1,0]
	v_pk_mul_f32 v[104:105], v[100:101], v[108:109] op_sel_hi:[1,0]
	s_waitcnt lgkmcnt(2)
	v_mfma_f32_16x16x32_bf16 v[88:91], v[88:91], v[28:31], v[96:99]
	v_fmac_f32_e32 v131, v129, v108
	v_mov_b64_e32 v[110:111], v[66:67]
	v_mov_b64_e32 v[108:109], v[64:65]
	s_waitcnt lgkmcnt(0)
	v_mfma_f32_16x16x32_bf16 v[28:31], v[92:95], v[28:31], v[104:107]
	ds_read_b64_tr_b16 v[94:95], v193 offset:11520
	ds_read_b64_tr_b16 v[92:93], v193 offset:9216
	ds_read_b64_tr_b16 v[96:97], v193 offset:9248
	ds_read_b64_tr_b16 v[98:99], v193 offset:11552
	s_waitcnt lgkmcnt(2)
	v_mfma_f32_16x16x32_bf16 v[92:95], v[92:95], v[32:35], v[68:71]
	s_nop 2
	ds_read_b64_tr_b16 v[68:69], v193 offset:9280
	ds_read_b64_tr_b16 v[70:71], v193 offset:11584
	s_waitcnt lgkmcnt(0)
	v_mfma_f32_16x16x32_bf16 v[104:107], v[68:71], v[32:35], v[88:91]
	ds_read_b64_tr_b16 v[68:69], v193 offset:9312
	ds_read_b64_tr_b16 v[70:71], v193 offset:11616
	s_nop 0
	v_mov_b64_e32 v[90:91], v[62:63]
	v_mov_b64_e32 v[88:89], v[60:61]
	v_mfma_f32_16x16x32_bf16 v[96:99], v[96:99], v[32:35], v[76:79]
	s_waitcnt lgkmcnt(0)
	v_mfma_f32_16x16x32_bf16 v[112:115], v[68:71], v[32:35], v[28:31]
	v_mov_b64_e32 v[70:71], v[54:55]
	v_mov_b64_e32 v[78:79], v[58:59]
	v_mov_b64_e32 v[68:69], v[52:53]
	v_mov_b64_e32 v[76:77], v[56:57]

.LBB0_542:
	ds_read_b128 v[108:111], v191
	ds_read_b128 v[112:115], v191 offset:64
	s_waitcnt lgkmcnt(1)
	v_mfma_f32_16x16x32_bf16 v[68:71], v[108:111], v[4:7], v[68:71]
	v_mfma_f32_16x16x32_bf16 v[76:79], v[108:111], v[12:15], v[76:79]
	s_waitcnt lgkmcnt(0)
	v_mfma_f32_16x16x32_bf16 v[108:111], v[112:115], v[8:11], v[68:71]
	s_nop 4
	ds_read_b128 v[68:71], v191 offset:2304
	s_waitcnt lgkmcnt(0)
	v_mfma_f32_16x16x32_bf16 v[28:31], v[68:71], v[4:7], v[28:31]
	v_mfma_f32_16x16x32_bf16 v[68:71], v[68:71], v[12:15], v[88:91]
	s_nop 2
	ds_read_b128 v[88:91], v191 offset:2368
	s_waitcnt lgkmcnt(0)
	v_mfma_f32_16x16x32_bf16 v[28:31], v[88:91], v[8:11], v[28:31]
	v_mfma_f32_16x16x32_bf16 v[88:91], v[88:91], v[16:19], v[68:71]
	s_nop 2
	ds_read_b128 v[68:71], v191 offset:4608
	s_waitcnt lgkmcnt(0)
	v_mfma_f32_16x16x32_bf16 v[92:95], v[68:71], v[4:7], v[92:95]
	v_mfma_f32_16x16x32_bf16 v[68:71], v[68:71], v[12:15], v[104:107]
	s_nop 2
	ds_read_b128 v[104:107], v191 offset:4672
	s_waitcnt lgkmcnt(0)
	v_mfma_f32_16x16x32_bf16 v[134:137], v[104:107], v[8:11], v[92:95]
	s_nop 2
	ds_read_b128 v[92:95], v191 offset:6976
	v_mfma_f32_16x16x32_bf16 v[104:107], v[104:107], v[16:19], v[68:71]
	s_nop 2
	ds_read_b128 v[68:71], v191 offset:6912
	s_waitcnt lgkmcnt(0)
	v_mfma_f32_16x16x32_bf16 v[32:35], v[68:71], v[4:7], v[32:35]
	v_mfma_f32_16x16x32_bf16 v[68:71], v[68:71], v[12:15], v[96:99]
	v_mfma_f32_16x16x32_bf16 v[138:141], v[92:95], v[8:11], v[32:35]
	s_nop 5
	v_max_f32_e32 v3, v110, v111
	v_max_f32_e32 v32, v30, v31
	v_max_f32_e32 v33, v134, v135
	v_mfma_f32_16x16x32_bf16 v[92:95], v[92:95], v[16:19], v[68:71]
	v_max_f32_e32 v34, v136, v137
	v_max3_f32 v3, v108, v109, v3
	v_max_f32_e32 v35, v140, v141
	v_max3_f32 v35, v138, v139, v35
	v_max3_f32 v32, v28, v29, v32
	v_max3_f32 v33, v33, v34, v35
	v_max3_f32 v3, v3, v32, v33
	v_mov_b32_e32 v32, v3
	s_nop 1
	v_permlane32_swap_b32_e32 v3, v32
	v_max_f32_e32 v3, v3, v32
	v_mov_b32_e32 v32, v3
	s_nop 1
	v_permlane16_swap_b32_e32 v3, v32
	v_max3_f32 v132, v218, v3, v32
	v_sub_f32_e32 v3, v218, v132
	v_mfma_f32_16x16x32_bf16 v[76:79], v[112:115], v[16:19], v[76:79]
	v_exp_f32_e32 v112, v3
	v_sub_f32_e32 v3, v108, v132
	v_pk_mul_f32 v[96:97], v[72:73], v[112:113] op_sel_hi:[1,0]
	v_pk_mul_f32 v[72:73], v[80:81], v[112:113] op_sel_hi:[1,0]
	v_exp_f32_e32 v80, v3
	v_sub_f32_e32 v3, v109, v132
	v_pk_mul_f32 v[98:99], v[74:75], v[112:113] op_sel_hi:[1,0]
	v_pk_mul_f32 v[74:75], v[82:83], v[112:113] op_sel_hi:[1,0]
	v_exp_f32_e32 v82, v3
	v_sub_f32_e32 v3, v110, v132
	v_exp_f32_e32 v81, v3
	v_sub_f32_e32 v3, v111, v132
	v_exp_f32_e32 v83, v3
	v_sub_f32_e32 v3, v28, v132
	v_exp_f32_e32 v28, v3
	v_sub_f32_e32 v3, v29, v132
	v_pk_mul_f32 v[68:69], v[84:85], v[112:113] op_sel_hi:[1,0]
	v_exp_f32_e32 v84, v3
	v_sub_f32_e32 v3, v30, v132
	v_exp_f32_e32 v29, v3
	v_sub_f32_e32 v3, v31, v132
	v_exp_f32_e32 v85, v3
	v_sub_f32_e32 v3, v134, v132
	v_exp_f32_e32 v30, v3
	v_sub_f32_e32 v3, v135, v132
	v_pk_mul_f32 v[70:71], v[86:87], v[112:113] op_sel_hi:[1,0]
	v_exp_f32_e32 v86, v3
	v_sub_f32_e32 v3, v136, v132
	v_exp_f32_e32 v31, v3
	v_sub_f32_e32 v3, v137, v132
	v_exp_f32_e32 v87, v3
	v_sub_f32_e32 v3, v138, v132
	v_pk_mul_f32 v[32:33], v[100:101], v[112:113] op_sel_hi:[1,0]
	v_exp_f32_e32 v100, v3
	v_sub_f32_e32 v3, v139, v132
	v_pk_mul_f32 v[34:35], v[102:103], v[112:113] op_sel_hi:[1,0]
	v_exp_f32_e32 v102, v3
	v_sub_f32_e32 v3, v140, v132
	v_exp_f32_e32 v101, v3
	v_sub_f32_e32 v3, v141, v132
	v_exp_f32_e32 v103, v3
	v_pk_add_f32 v[108:109], v[80:81], 0 op_sel_hi:[1,0]
	v_pk_add_f32 v[110:111], v[84:85], v[82:83]
	v_cvt_pk_bf16_f32 v80, v80, v82
	v_cvt_pk_bf16_f32 v81, v81, v83
	v_cvt_pk_bf16_f32 v82, v28, v84
	v_cvt_pk_bf16_f32 v83, v29, v85
	v_max_f32_e32 v3, v78, v79
	v_pk_add_f32 v[108:109], v[28:29], v[108:109]
	v_pk_add_f32 v[110:111], v[86:87], v[110:111]
	v_cvt_pk_bf16_f32 v28, v30, v86
	v_max_f32_e32 v84, v90, v91
	v_pk_add_f32 v[108:109], v[30:31], v[108:109]
	v_cvt_pk_bf16_f32 v29, v31, v87
	v_max_f32_e32 v85, v104, v105
	v_pk_add_f32 v[108:109], v[100:101], v[108:109]
	v_cvt_pk_bf16_f32 v30, v100, v102
	v_max_f32_e32 v86, v106, v107
	v_max_f32_e32 v87, v94, v95
	v_max3_f32 v87, v92, v93, v87
	v_max3_f32 v3, v76, v77, v3
	v_max3_f32 v84, v88, v89, v84
	v_max3_f32 v85, v85, v86, v87
	v_max3_f32 v3, v3, v84, v85
	v_mov_b32_e32 v84, v3
	s_nop 1
	v_permlane32_swap_b32_e32 v3, v84
	v_max_f32_e32 v3, v3, v84
	v_mov_b32_e32 v84, v3
	s_nop 1
	v_permlane16_swap_b32_e32 v3, v84
	v_max3_f32 v134, v217, v3, v84
	v_pk_add_f32 v[110:111], v[102:103], v[110:111]
	v_sub_f32_e32 v3, v217, v134
	v_pk_add_f32 v[108:109], v[108:109], v[110:111]
	v_exp_f32_e32 v110, v3
	v_sub_f32_e32 v3, v76, v134
	v_cvt_pk_bf16_f32 v31, v101, v103
	v_pk_mul_f32 v[84:85], v[52:53], v[110:111] op_sel_hi:[1,0]
	v_exp_f32_e32 v52, v3
	v_sub_f32_e32 v3, v77, v134
	v_exp_f32_e32 v53, v3
	v_sub_f32_e32 v3, v78, v134
	v_pk_mul_f32 v[86:87], v[54:55], v[110:111] op_sel_hi:[1,0]
	v_exp_f32_e32 v54, v3
	v_sub_f32_e32 v3, v79, v134
	v_exp_f32_e32 v55, v3
	v_sub_f32_e32 v3, v88, v134
	v_pk_mul_f32 v[102:103], v[58:59], v[110:111] op_sel_hi:[1,0]
	v_pk_mul_f32 v[58:59], v[66:67], v[110:111] op_sel_hi:[1,0]
	v_exp_f32_e32 v66, v3
	v_sub_f32_e32 v3, v89, v134
	v_exp_f32_e32 v67, v3
	v_sub_f32_e32 v3, v90, v134
	v_exp_f32_e32 v76, v3
	v_sub_f32_e32 v3, v91, v134
	v_exp_f32_e32 v77, v3
	v_sub_f32_e32 v3, v104, v134
	v_exp_f32_e32 v78, v3
	v_sub_f32_e32 v3, v105, v134
	v_exp_f32_e32 v79, v3
	v_sub_f32_e32 v3, v106, v134
	v_exp_f32_e32 v88, v3
	v_sub_f32_e32 v3, v107, v134
	v_exp_f32_e32 v89, v3
	v_sub_f32_e32 v3, v92, v134
	v_exp_f32_e32 v90, v3
	v_sub_f32_e32 v3, v93, v134
	v_exp_f32_e32 v91, v3
	v_sub_f32_e32 v3, v94, v134
	v_exp_f32_e32 v92, v3
	v_sub_f32_e32 v3, v95, v134
	v_exp_f32_e32 v93, v3
	v_pk_mul_f32 v[100:101], v[56:57], v[110:111] op_sel_hi:[1,0]
	v_pk_mul_f32 v[56:57], v[64:65], v[110:111] op_sel_hi:[1,0]
	v_pk_add_f32 v[64:65], v[66:67], v[52:53]
	v_pk_add_f32 v[94:95], v[76:77], v[54:55]
	v_pk_add_f32 v[64:65], v[78:79], v[64:65]
	v_pk_add_f32 v[94:95], v[88:89], v[94:95]
	v_pk_add_f32 v[64:65], v[90:91], v[64:65]
	v_pk_add_f32 v[94:95], v[92:93], v[94:95]
	v_pk_add_f32 v[64:65], v[64:65], v[64:65] op_sel:[0,1] op_sel_hi:[1,0]
	v_pk_add_f32 v[94:95], v[94:95], v[94:95] op_sel:[0,1] op_sel_hi:[1,0]
	v_mov_b32_e32 v65, v108
	v_mov_b32_e32 v95, v109
	v_pk_mul_f32 v[62:63], v[62:63], v[110:111] op_sel_hi:[1,0]
	v_pk_mul_f32 v[60:61], v[60:61], v[110:111] op_sel_hi:[1,0]
	v_mov_b32_e32 v111, v112
	v_pk_add_f32 v[64:65], v[64:65], v[94:95]
	s_nop 0
	v_pk_fma_f32 v[130:131], v[128:129], v[110:111], v[64:65]
	v_cvt_pk_bf16_f32 v64, v52, v53
	v_cvt_pk_bf16_f32 v65, v54, v55
	v_cvt_pk_bf16_f32 v66, v66, v67
	v_cvt_pk_bf16_f32 v67, v76, v77
	v_cvt_pk_bf16_f32 v52, v78, v79
	v_cvt_pk_bf16_f32 v53, v88, v89
	v_cvt_pk_bf16_f32 v54, v90, v91
	v_cvt_pk_bf16_f32 v55, v92, v93
	ds_read_b64_tr_b16 v[78:79], v192 offset:11520
	ds_read_b64_tr_b16 v[76:77], v192 offset:9216
	ds_read_b64_tr_b16 v[88:89], v192 offset:9248
	ds_read_b64_tr_b16 v[90:91], v192 offset:11552
	s_waitcnt lgkmcnt(2)
	v_mfma_f32_16x16x32_bf16 v[92:95], v[76:79], v[80:83], v[96:99]
	v_mfma_f32_16x16x32_bf16 v[76:79], v[76:79], v[64:67], v[84:87]
	s_waitcnt lgkmcnt(0)
	v_mfma_f32_16x16x32_bf16 v[72:75], v[88:91], v[80:83], v[72:75]
	v_mfma_f32_16x16x32_bf16 v[84:87], v[88:91], v[64:67], v[100:103]
	ds_read_b64_tr_b16 v[88:89], v192 offset:9280
	ds_read_b64_tr_b16 v[90:91], v192 offset:11584
	s_waitcnt lgkmcnt(0)
	v_mfma_f32_16x16x32_bf16 v[100:103], v[88:91], v[80:83], v[68:71]
	s_nop 2
	ds_read_b64_tr_b16 v[68:69], v192 offset:9312
	ds_read_b64_tr_b16 v[70:71], v192 offset:11616
	v_mfma_f32_16x16x32_bf16 v[60:63], v[88:91], v[64:67], v[60:63]
	s_waitcnt lgkmcnt(0)
	v_mfma_f32_16x16x32_bf16 v[32:35], v[68:71], v[80:83], v[32:35]
	v_mfma_f32_16x16x32_bf16 v[56:59], v[68:71], v[64:67], v[56:59]
	ds_read_b64_tr_b16 v[66:67], v193 offset:11520
	ds_read_b64_tr_b16 v[64:65], v193 offset:9216
	ds_read_b64_tr_b16 v[80:81], v193 offset:9248
	ds_read_b64_tr_b16 v[82:83], v193 offset:11552
	s_waitcnt lgkmcnt(2)
	v_mfma_f32_16x16x32_bf16 v[92:95], v[64:67], v[28:31], v[92:95]
	v_mfma_f32_16x16x32_bf16 v[68:71], v[64:67], v[52:55], v[76:79]
	ds_read_b64_tr_b16 v[64:65], v193 offset:9280
	ds_read_b64_tr_b16 v[66:67], v193 offset:11584
	s_waitcnt lgkmcnt(0)
	v_mfma_f32_16x16x32_bf16 v[88:91], v[64:67], v[52:55], v[60:63]
	s_nop 2
	ds_read_b64_tr_b16 v[60:61], v193 offset:9312
	ds_read_b64_tr_b16 v[62:63], v193 offset:11616
	v_mfma_f32_16x16x32_bf16 v[96:99], v[80:83], v[28:31], v[72:75]
	v_mfma_f32_16x16x32_bf16 v[76:79], v[80:83], v[52:55], v[84:87]
	v_mfma_f32_16x16x32_bf16 v[104:107], v[64:67], v[28:31], v[100:103]
	s_waitcnt lgkmcnt(0)
	v_mfma_f32_16x16x32_bf16 v[112:115], v[60:63], v[28:31], v[32:35]
	v_mfma_f32_16x16x32_bf16 v[108:111], v[60:63], v[52:55], v[56:59]

.LBB0_554:
	ds_read_b128 v[60:63], v191 offset:18432
	v_mov_b32_e32 v129, v131
	s_waitcnt lgkmcnt(0)
	v_mfma_f32_16x16x32_bf16 v[24:27], v[60:63], v[12:15], v[24:27]
	ds_read_b128 v[60:63], v191 offset:18496
	s_waitcnt lgkmcnt(0)
	v_mfma_f32_16x16x32_bf16 v[24:27], v[60:63], v[16:19], v[24:27]
	ds_read_b128 v[60:63], v191 offset:20736
	s_nop 6
	s_waitcnt lgkmcnt(0)
	v_mfma_f32_16x16x32_bf16 v[20:23], v[60:63], v[12:15], v[20:23]
	ds_read_b128 v[60:63], v191 offset:20800
	s_waitcnt lgkmcnt(0)
	v_mfma_f32_16x16x32_bf16 v[20:23], v[60:63], v[16:19], v[20:23]
	ds_read_b128 v[60:63], v191 offset:23040
	s_waitcnt lgkmcnt(0)
	v_mfma_f32_16x16x32_bf16 v[56:59], v[60:63], v[12:15], v[56:59]
	ds_read_b128 v[60:63], v191 offset:23104
	s_waitcnt lgkmcnt(0)
	v_mfma_f32_16x16x32_bf16 v[56:59], v[60:63], v[16:19], v[56:59]
	ds_read_b128 v[60:63], v191 offset:25344
	s_waitcnt lgkmcnt(0)
	v_mfma_f32_16x16x32_bf16 v[52:55], v[60:63], v[12:15], v[52:55]
	ds_read_b128 v[60:63], v191 offset:25408
	s_waitcnt lgkmcnt(0)
	v_mfma_f32_16x16x32_bf16 v[52:55], v[60:63], v[16:19], v[52:55]
	v_max_f32_e32 v3, v26, v27
	v_max_f32_e32 v60, v22, v23
	v_max_f32_e32 v61, v56, v57
	v_max_f32_e32 v62, v58, v59
	s_nop 3
	v_max_f32_e32 v63, v54, v55
	v_max3_f32 v63, v52, v53, v63
	v_max3_f32 v3, v24, v25, v3
	v_max3_f32 v60, v20, v21, v60
	v_max3_f32 v61, v61, v62, v63
	v_max3_f32 v3, v3, v60, v61
	v_mov_b32_e32 v60, v3
	s_nop 1
	v_permlane32_swap_b32_e32 v3, v60
	v_max_f32_e32 v3, v3, v60
	v_mov_b32_e32 v60, v3
	s_nop 1
	v_permlane16_swap_b32_e32 v3, v60
	v_max3_f32 v3, v134, v3, v60
	v_sub_f32_e32 v25, v25, v3
	v_exp_f32_e32 v86, v25
	v_sub_f32_e32 v25, v26, v3
	v_sub_f32_e32 v26, v27, v3
	v_sub_f32_e32 v20, v20, v3
	v_exp_f32_e32 v87, v26
	v_exp_f32_e32 v26, v20
	v_sub_f32_e32 v20, v21, v3
	v_exp_f32_e32 v100, v20
	v_sub_f32_e32 v20, v22, v3
	v_exp_f32_e32 v27, v20
	v_sub_f32_e32 v20, v23, v3
	v_exp_f32_e32 v101, v20
	v_sub_f32_e32 v20, v56, v3
	v_exp_f32_e32 v56, v20
	v_sub_f32_e32 v20, v57, v3
	v_exp_f32_e32 v102, v20
	v_sub_f32_e32 v20, v58, v3
	v_exp_f32_e32 v57, v20
	v_sub_f32_e32 v20, v59, v3
	v_sub_f32_e32 v24, v24, v3
	v_exp_f32_e32 v103, v20
	v_sub_f32_e32 v20, v52, v3
	v_exp_f32_e32 v24, v24
	v_exp_f32_e32 v25, v25
	v_exp_f32_e32 v52, v20
	v_sub_f32_e32 v20, v53, v3
	v_exp_f32_e32 v58, v20
	v_sub_f32_e32 v20, v54, v3
	v_exp_f32_e32 v53, v20
	v_sub_f32_e32 v20, v55, v3
	v_exp_f32_e32 v59, v20
	v_pk_add_f32 v[20:21], v[26:27], v[24:25]
	v_pk_add_f32 v[22:23], v[100:101], v[86:87]
	v_pk_add_f32 v[20:21], v[56:57], v[20:21]
	v_pk_add_f32 v[22:23], v[102:103], v[22:23]
	v_pk_add_f32 v[20:21], v[52:53], v[20:21]
	v_pk_add_f32 v[22:23], v[58:59], v[22:23]
	v_sub_f32_e32 v60, v134, v3
	v_pk_add_f32 v[20:21], v[20:21], v[22:23]
	v_exp_f32_e32 v84, v60
	v_add_f32_e32 v128, v20, v21
	v_cvt_pk_bf16_f32 v20, v24, v86
	v_cvt_pk_bf16_f32 v21, v25, v87
	v_cvt_pk_bf16_f32 v22, v26, v100
	v_cvt_pk_bf16_f32 v23, v27, v101
	v_cvt_pk_bf16_f32 v24, v56, v102
	v_cvt_pk_bf16_f32 v25, v57, v103
	v_cvt_pk_bf16_f32 v26, v52, v58
	v_cvt_pk_bf16_f32 v27, v53, v59
	ds_read_b64_tr_b16 v[54:55], v192 offset:29952
	ds_read_b64_tr_b16 v[52:53], v192 offset:27648
	ds_read_b64_tr_b16 v[56:57], v192 offset:27680
	ds_read_b64_tr_b16 v[58:59], v192 offset:29984
	v_pk_mul_f32 v[62:63], v[70:71], v[84:85] op_sel_hi:[1,0]
	v_pk_mul_f32 v[60:61], v[68:69], v[84:85] op_sel_hi:[1,0]
	v_pk_mul_f32 v[66:67], v[78:79], v[84:85] op_sel_hi:[1,0]
	v_pk_mul_f32 v[64:65], v[76:77], v[84:85] op_sel_hi:[1,0]
	s_waitcnt lgkmcnt(2)
	v_mfma_f32_16x16x32_bf16 v[52:55], v[52:55], v[20:23], v[60:63]
	s_nop 2
	ds_read_b64_tr_b16 v[60:61], v192 offset:27712
	ds_read_b64_tr_b16 v[62:63], v192 offset:30016
	v_pk_mul_f32 v[74:75], v[90:91], v[84:85] op_sel_hi:[1,0]
	v_pk_mul_f32 v[72:73], v[88:89], v[84:85] op_sel_hi:[1,0]
	s_waitcnt lgkmcnt(2)
	v_mfma_f32_16x16x32_bf16 v[56:59], v[56:59], v[20:23], v[64:67]
	s_nop 2
	ds_read_b64_tr_b16 v[64:65], v192 offset:27744
	ds_read_b64_tr_b16 v[66:67], v192 offset:30048
	v_pk_mul_f32 v[82:83], v[110:111], v[84:85] op_sel_hi:[1,0]
	v_pk_mul_f32 v[80:81], v[108:109], v[84:85] op_sel_hi:[1,0]
	s_waitcnt lgkmcnt(2)
	v_mfma_f32_16x16x32_bf16 v[60:63], v[60:63], v[20:23], v[72:75]
	v_fmac_f32_e32 v128, v130, v84
	s_waitcnt lgkmcnt(0)
	v_mfma_f32_16x16x32_bf16 v[20:23], v[64:67], v[20:23], v[80:83]
	ds_read_b64_tr_b16 v[66:67], v193 offset:29952
	ds_read_b64_tr_b16 v[64:65], v193 offset:27648
	ds_read_b64_tr_b16 v[72:73], v193 offset:27680
	ds_read_b64_tr_b16 v[74:75], v193 offset:29984
	s_waitcnt lgkmcnt(2)
	v_mfma_f32_16x16x32_bf16 v[52:55], v[64:67], v[24:27], v[52:55]
	ds_read_b64_tr_b16 v[64:65], v193 offset:27712
	ds_read_b64_tr_b16 v[66:67], v193 offset:30016
	s_waitcnt lgkmcnt(0)
	v_mfma_f32_16x16x32_bf16 v[60:63], v[64:67], v[24:27], v[60:63]
	ds_read_b64_tr_b16 v[64:65], v193 offset:27744
	ds_read_b64_tr_b16 v[66:67], v193 offset:30048
	v_mfma_f32_16x16x32_bf16 v[56:59], v[72:75], v[24:27], v[56:59]
	s_waitcnt lgkmcnt(0)
	v_mfma_f32_16x16x32_bf16 v[84:87], v[64:67], v[24:27], v[20:23]

.LBB0_565:
	ds_read_b128 v[60:63], v191 offset:18432
	v_mov_b32_e32 v128, v130
	s_waitcnt lgkmcnt(0)
	v_mfma_f32_16x16x32_bf16 v[24:27], v[60:63], v[4:7], v[24:27]
	ds_read_b128 v[60:63], v191 offset:18496
	s_waitcnt lgkmcnt(0)
	v_mfma_f32_16x16x32_bf16 v[24:27], v[60:63], v[8:11], v[24:27]
	ds_read_b128 v[60:63], v191 offset:20736
	s_nop 6
	s_waitcnt lgkmcnt(0)
	v_mfma_f32_16x16x32_bf16 v[20:23], v[60:63], v[4:7], v[20:23]
	ds_read_b128 v[60:63], v191 offset:20800
	s_waitcnt lgkmcnt(0)
	v_mfma_f32_16x16x32_bf16 v[20:23], v[60:63], v[8:11], v[20:23]
	ds_read_b128 v[60:63], v191 offset:23040
	s_waitcnt lgkmcnt(0)
	v_mfma_f32_16x16x32_bf16 v[56:59], v[60:63], v[4:7], v[56:59]
	ds_read_b128 v[60:63], v191 offset:23104
	s_waitcnt lgkmcnt(0)
	v_mfma_f32_16x16x32_bf16 v[56:59], v[60:63], v[8:11], v[56:59]
	ds_read_b128 v[60:63], v191 offset:25344
	s_waitcnt lgkmcnt(0)
	v_mfma_f32_16x16x32_bf16 v[52:55], v[60:63], v[4:7], v[52:55]
	ds_read_b128 v[60:63], v191 offset:25408
	s_waitcnt lgkmcnt(0)
	v_mfma_f32_16x16x32_bf16 v[52:55], v[60:63], v[8:11], v[52:55]
	v_max_f32_e32 v3, v26, v27
	v_max_f32_e32 v60, v22, v23
	v_max_f32_e32 v61, v56, v57
	v_max_f32_e32 v62, v58, v59
	s_nop 3
	v_max_f32_e32 v63, v54, v55
	v_max3_f32 v63, v52, v53, v63
	v_max3_f32 v3, v24, v25, v3
	v_max3_f32 v60, v20, v21, v60
	v_max3_f32 v61, v61, v62, v63
	v_max3_f32 v3, v3, v60, v61
	v_mov_b32_e32 v60, v3
	s_nop 1
	v_permlane32_swap_b32_e32 v3, v60
	v_max_f32_e32 v3, v3, v60
	v_mov_b32_e32 v60, v3
	s_nop 1
	v_permlane16_swap_b32_e32 v3, v60
	v_max3_f32 v217, v132, v3, v60
	v_sub_f32_e32 v3, v132, v217
	v_exp_f32_e32 v84, v3
	v_sub_f32_e32 v3, v24, v217
	v_exp_f32_e32 v24, v3
	v_sub_f32_e32 v3, v25, v217
	v_exp_f32_e32 v86, v3
	v_sub_f32_e32 v3, v26, v217
	v_exp_f32_e32 v25, v3
	v_sub_f32_e32 v3, v27, v217
	v_exp_f32_e32 v87, v3
	v_sub_f32_e32 v3, v20, v217
	v_exp_f32_e32 v26, v3
	v_sub_f32_e32 v3, v21, v217
	v_exp_f32_e32 v100, v3
	v_sub_f32_e32 v3, v22, v217
	v_exp_f32_e32 v27, v3
	v_sub_f32_e32 v3, v23, v217
	v_exp_f32_e32 v101, v3
	v_sub_f32_e32 v3, v56, v217
	v_exp_f32_e32 v56, v3
	v_sub_f32_e32 v3, v57, v217
	v_exp_f32_e32 v102, v3
	v_sub_f32_e32 v3, v58, v217
	v_exp_f32_e32 v57, v3
	v_sub_f32_e32 v3, v59, v217
	v_exp_f32_e32 v103, v3
	v_sub_f32_e32 v3, v52, v217
	v_exp_f32_e32 v52, v3
	v_sub_f32_e32 v3, v53, v217
	v_exp_f32_e32 v58, v3
	v_sub_f32_e32 v3, v54, v217
	v_exp_f32_e32 v53, v3
	v_sub_f32_e32 v3, v55, v217
	v_exp_f32_e32 v59, v3
	v_pk_add_f32 v[20:21], v[26:27], v[24:25]
	v_pk_add_f32 v[22:23], v[100:101], v[86:87]
	v_pk_add_f32 v[20:21], v[56:57], v[20:21]
	v_pk_add_f32 v[22:23], v[102:103], v[22:23]
	v_pk_add_f32 v[20:21], v[52:53], v[20:21]
	v_pk_add_f32 v[22:23], v[58:59], v[22:23]
	v_pk_mul_f32 v[62:63], v[94:95], v[84:85] op_sel_hi:[1,0]
	v_pk_add_f32 v[20:21], v[20:21], v[22:23]
	v_pk_mul_f32 v[60:61], v[92:93], v[84:85] op_sel_hi:[1,0]
	v_add_f32_e32 v129, v20, v21
	v_cvt_pk_bf16_f32 v20, v24, v86
	v_cvt_pk_bf16_f32 v21, v25, v87
	v_cvt_pk_bf16_f32 v22, v26, v100
	v_cvt_pk_bf16_f32 v23, v27, v101
	v_cvt_pk_bf16_f32 v24, v56, v102
	v_cvt_pk_bf16_f32 v25, v57, v103
	v_cvt_pk_bf16_f32 v26, v52, v58
	v_cvt_pk_bf16_f32 v27, v53, v59
	ds_read_b64_tr_b16 v[54:55], v192 offset:29952
	ds_read_b64_tr_b16 v[52:53], v192 offset:27648
	ds_read_b64_tr_b16 v[56:57], v192 offset:27680
	ds_read_b64_tr_b16 v[58:59], v192 offset:29984
	v_pk_mul_f32 v[66:67], v[98:99], v[84:85] op_sel_hi:[1,0]
	v_pk_mul_f32 v[64:65], v[96:97], v[84:85] op_sel_hi:[1,0]
	s_waitcnt lgkmcnt(2)
	v_mfma_f32_16x16x32_bf16 v[52:55], v[52:55], v[20:23], v[60:63]
	s_nop 2
	ds_read_b64_tr_b16 v[60:61], v192 offset:27712
	ds_read_b64_tr_b16 v[62:63], v192 offset:30016
	v_pk_mul_f32 v[74:75], v[106:107], v[84:85] op_sel_hi:[1,0]
	v_pk_mul_f32 v[72:73], v[104:105], v[84:85] op_sel_hi:[1,0]
	s_waitcnt lgkmcnt(2)
	v_mfma_f32_16x16x32_bf16 v[56:59], v[56:59], v[20:23], v[64:67]
	s_nop 2
	ds_read_b64_tr_b16 v[64:65], v192 offset:27744
	ds_read_b64_tr_b16 v[66:67], v192 offset:30048
	v_pk_mul_f32 v[82:83], v[114:115], v[84:85] op_sel_hi:[1,0]
	v_pk_mul_f32 v[80:81], v[112:113], v[84:85] op_sel_hi:[1,0]
	s_waitcnt lgkmcnt(2)
	v_mfma_f32_16x16x32_bf16 v[60:63], v[60:63], v[20:23], v[72:75]
	v_fmac_f32_e32 v129, v131, v84
	v_mov_b64_e32 v[84:85], v[108:109]
	v_mov_b32_e32 v3, v134
	s_waitcnt lgkmcnt(0)
	v_mfma_f32_16x16x32_bf16 v[20:23], v[64:67], v[20:23], v[80:83]
	ds_read_b64_tr_b16 v[66:67], v193 offset:29952
	ds_read_b64_tr_b16 v[64:65], v193 offset:27648
	ds_read_b64_tr_b16 v[72:73], v193 offset:27680
	ds_read_b64_tr_b16 v[74:75], v193 offset:29984
	v_mov_b64_e32 v[86:87], v[110:111]
	s_waitcnt lgkmcnt(2)
	v_mfma_f32_16x16x32_bf16 v[64:67], v[64:67], v[24:27], v[52:55]
	s_nop 2
	ds_read_b64_tr_b16 v[52:53], v193 offset:27712
	ds_read_b64_tr_b16 v[54:55], v193 offset:30016
	s_waitcnt lgkmcnt(0)
	v_mfma_f32_16x16x32_bf16 v[80:83], v[52:55], v[24:27], v[60:63]
	ds_read_b64_tr_b16 v[52:53], v193 offset:27744
	ds_read_b64_tr_b16 v[54:55], v193 offset:30048
	s_nop 0
	v_mov_b64_e32 v[60:61], v[88:89]
	v_mov_b64_e32 v[62:63], v[90:91]
	v_mfma_f32_16x16x32_bf16 v[72:75], v[72:75], v[24:27], v[56:59]
	s_waitcnt lgkmcnt(0)
	v_mfma_f32_16x16x32_bf16 v[100:103], v[52:55], v[24:27], v[20:23]
	v_mov_b64_e32 v[52:53], v[68:69]
	v_mov_b64_e32 v[56:57], v[76:77]
	v_mov_b64_e32 v[54:55], v[70:71]
	v_mov_b64_e32 v[58:59], v[78:79]

.LBB0_584:
	ds_read_b128 v[80:83], v191 offset:18432
	ds_read_b128 v[84:87], v191 offset:18496
	s_waitcnt lgkmcnt(1)
	v_mfma_f32_16x16x32_bf16 v[52:55], v[80:83], v[4:7], v[52:55]
	v_mfma_f32_16x16x32_bf16 v[80:83], v[80:83], v[12:15], v[60:63]
	s_waitcnt lgkmcnt(0)
	v_mfma_f32_16x16x32_bf16 v[60:63], v[84:87], v[8:11], v[52:55]
	s_nop 4
	ds_read_b128 v[52:55], v191 offset:20736
	s_waitcnt lgkmcnt(0)
	v_mfma_f32_16x16x32_bf16 v[20:23], v[52:55], v[4:7], v[20:23]
	v_mfma_f32_16x16x32_bf16 v[52:55], v[52:55], v[12:15], v[64:67]
	s_nop 2
	ds_read_b128 v[64:67], v191 offset:20800
	v_mfma_f32_16x16x32_bf16 v[80:83], v[84:87], v[16:19], v[80:83]
	s_waitcnt lgkmcnt(0)
	v_mfma_f32_16x16x32_bf16 v[84:87], v[64:67], v[16:19], v[52:55]
	s_nop 2
	ds_read_b128 v[52:55], v191 offset:23040
	v_mfma_f32_16x16x32_bf16 v[20:23], v[64:67], v[8:11], v[20:23]
	ds_read_b128 v[64:67], v191 offset:23104
	s_waitcnt lgkmcnt(1)
	v_mfma_f32_16x16x32_bf16 v[56:59], v[52:55], v[4:7], v[56:59]
	v_mfma_f32_16x16x32_bf16 v[52:55], v[52:55], v[12:15], v[100:103]
	s_waitcnt lgkmcnt(0)
	v_mfma_f32_16x16x32_bf16 v[100:103], v[64:67], v[16:19], v[52:55]
	v_mfma_f32_16x16x32_bf16 v[146:149], v[64:67], v[8:11], v[56:59]
	s_nop 4
	ds_read_b128 v[52:55], v191 offset:25344
	ds_read_b128 v[56:59], v191 offset:25408
	s_waitcnt lgkmcnt(1)
	v_mfma_f32_16x16x32_bf16 v[24:27], v[52:55], v[4:7], v[24:27]
	v_mfma_f32_16x16x32_bf16 v[52:55], v[52:55], v[12:15], v[72:75]
	s_waitcnt lgkmcnt(0)
	v_mfma_f32_16x16x32_bf16 v[154:157], v[56:59], v[8:11], v[24:27]
	s_nop 4
	v_max_f32_e32 v3, v62, v63
	v_max_f32_e32 v24, v22, v23
	v_max_f32_e32 v25, v146, v147
	v_mfma_f32_16x16x32_bf16 v[56:59], v[56:59], v[16:19], v[52:55]
	v_max_f32_e32 v26, v148, v149
	v_max3_f32 v3, v60, v61, v3
	v_max_f32_e32 v27, v156, v157
	v_max3_f32 v27, v154, v155, v27
	v_max3_f32 v24, v20, v21, v24
	v_max3_f32 v25, v25, v26, v27
	v_max3_f32 v3, v3, v24, v25
	v_mov_b32_e32 v24, v3
	s_nop 1
	v_permlane32_swap_b32_e32 v3, v24
	v_max_f32_e32 v3, v3, v24
	v_mov_b32_e32 v24, v3
	s_nop 1
	v_permlane16_swap_b32_e32 v3, v24
	v_max3_f32 v217, v132, v3, v24
	v_sub_f32_e32 v3, v132, v217
	v_exp_f32_e32 v128, v3
	v_sub_f32_e32 v3, v60, v217
	v_pk_mul_f32 v[52:53], v[104:105], v[128:129] op_sel_hi:[1,0]
	v_exp_f32_e32 v105, v3
	v_sub_f32_e32 v3, v61, v217
	v_pk_mul_f32 v[54:55], v[106:107], v[128:129] op_sel_hi:[1,0]
	v_exp_f32_e32 v107, v3
	v_sub_f32_e32 v3, v62, v217
	v_pk_mul_f32 v[24:25], v[112:113], v[128:129] op_sel_hi:[1,0]
	v_exp_f32_e32 v113, v3
	v_sub_f32_e32 v3, v63, v217
	v_pk_mul_f32 v[26:27], v[114:115], v[128:129] op_sel_hi:[1,0]
	v_exp_f32_e32 v115, v3
	v_sub_f32_e32 v3, v20, v217
	v_exp_f32_e32 v133, v3
	v_sub_f32_e32 v3, v21, v217
	v_exp_f32_e32 v135, v3
	v_sub_f32_e32 v3, v22, v217
	v_exp_f32_e32 v139, v3
	v_sub_f32_e32 v3, v23, v217
	v_exp_f32_e32 v143, v3
	v_sub_f32_e32 v3, v146, v217
	v_exp_f32_e32 v137, v3
	v_sub_f32_e32 v3, v147, v217
	v_exp_f32_e32 v141, v3
	v_sub_f32_e32 v3, v148, v217
	v_exp_f32_e32 v147, v3
	v_sub_f32_e32 v3, v149, v217
	v_exp_f32_e32 v149, v3
	v_sub_f32_e32 v3, v154, v217
	v_exp_f32_e32 v151, v3
	v_sub_f32_e32 v3, v155, v217
	v_exp_f32_e32 v153, v3
	v_sub_f32_e32 v3, v156, v217
	v_exp_f32_e32 v155, v3
	v_sub_f32_e32 v3, v157, v217
	v_pk_mul_f32 v[72:73], v[92:93], v[128:129] op_sel_hi:[1,0]
	v_exp_f32_e32 v157, v3
	v_max_f32_e32 v3, v82, v83
	v_pk_mul_f32 v[74:75], v[94:95], v[128:129] op_sel_hi:[1,0]
	v_max_f32_e32 v92, v86, v87
	v_max_f32_e32 v93, v100, v101
	v_pk_mul_f32 v[64:65], v[96:97], v[128:129] op_sel_hi:[1,0]
	v_max_f32_e32 v94, v102, v103
	v_max_f32_e32 v95, v58, v59
	v_max3_f32 v95, v56, v57, v95
	v_max3_f32 v3, v80, v81, v3
	v_max3_f32 v92, v84, v85, v92
	v_max3_f32 v93, v93, v94, v95
	v_max3_f32 v3, v3, v92, v93
	v_mov_b32_e32 v92, v3
	s_nop 1
	v_permlane32_swap_b32_e32 v3, v92
	v_max_f32_e32 v3, v3, v92
	v_mov_b32_e32 v92, v3
	s_nop 1
	v_permlane16_swap_b32_e32 v3, v92
	v_max3_f32 v3, v134, v3, v92
	v_sub_f32_e32 v92, v134, v3
	v_exp_f32_e32 v218, v92
	v_sub_f32_e32 v56, v56, v3
	v_sub_f32_e32 v58, v58, v3
	v_exp_f32_e32 v150, v56
	v_pk_mul_f32 v[92:93], v[76:77], v[218:219] op_sel_hi:[1,0]
	v_sub_f32_e32 v76, v80, v3
	v_exp_f32_e32 v104, v76
	v_sub_f32_e32 v76, v81, v3
	v_exp_f32_e32 v106, v76
	v_sub_f32_e32 v76, v82, v3
	v_exp_f32_e32 v112, v76
	v_sub_f32_e32 v76, v83, v3
	v_exp_f32_e32 v114, v76
	v_sub_f32_e32 v76, v84, v3
	v_exp_f32_e32 v132, v76
	v_sub_f32_e32 v76, v85, v3
	v_exp_f32_e32 v134, v76
	v_sub_f32_e32 v76, v86, v3
	v_exp_f32_e32 v138, v76
	v_sub_f32_e32 v76, v87, v3
	v_exp_f32_e32 v142, v76
	v_sub_f32_e32 v76, v100, v3
	v_exp_f32_e32 v136, v76
	v_sub_f32_e32 v76, v101, v3
	v_exp_f32_e32 v140, v76
	v_sub_f32_e32 v76, v102, v3
	v_exp_f32_e32 v146, v76
	v_sub_f32_e32 v76, v103, v3
	v_exp_f32_e32 v148, v76
	v_sub_f32_e32 v56, v57, v3
	v_exp_f32_e32 v154, v58
	v_sub_f32_e32 v58, v59, v3
	v_exp_f32_e32 v152, v56
	v_exp_f32_e32 v156, v58
	v_pk_mul_f32 v[94:95], v[78:79], v[218:219] op_sel_hi:[1,0]
	v_pk_add_f32 v[76:77], v[132:133], v[104:105]
	v_pk_add_f32 v[56:57], v[134:135], v[106:107]
	v_pk_add_f32 v[78:79], v[138:139], v[112:113]
	v_pk_add_f32 v[58:59], v[142:143], v[114:115]
	v_pk_add_f32 v[76:77], v[136:137], v[76:77]
	v_pk_add_f32 v[56:57], v[140:141], v[56:57]
	v_pk_add_f32 v[78:79], v[146:147], v[78:79]
	v_pk_add_f32 v[58:59], v[148:149], v[58:59]
	v_pk_add_f32 v[76:77], v[150:151], v[76:77]
	v_pk_add_f32 v[56:57], v[152:153], v[56:57]
	v_pk_add_f32 v[78:79], v[154:155], v[78:79]
	v_pk_add_f32 v[58:59], v[156:157], v[58:59]
	v_pk_add_f32 v[56:57], v[76:77], v[56:57]
	v_pk_add_f32 v[58:59], v[78:79], v[58:59]
	v_pk_mul_f32 v[66:67], v[98:99], v[128:129] op_sel_hi:[1,0]
	v_pk_mul_f32 v[98:99], v[70:71], v[218:219] op_sel_hi:[1,0]
	v_pk_mul_f32 v[96:97], v[68:69], v[218:219] op_sel_hi:[1,0]
	v_pk_mul_f32 v[90:91], v[90:91], v[218:219] op_sel_hi:[1,0]
	v_pk_mul_f32 v[88:89], v[88:89], v[218:219] op_sel_hi:[1,0]
	v_pk_mul_f32 v[70:71], v[110:111], v[218:219] op_sel_hi:[1,0]
	v_pk_mul_f32 v[68:69], v[108:109], v[218:219] op_sel_hi:[1,0]
	v_mov_b32_e32 v219, v128
	v_pk_add_f32 v[56:57], v[56:57], v[58:59]
	v_cvt_pk_bf16_f32 v60, v105, v107
	v_cvt_pk_bf16_f32 v61, v113, v115
	v_cvt_pk_bf16_f32 v62, v133, v135
	v_cvt_pk_bf16_f32 v63, v139, v143
	v_cvt_pk_bf16_f32 v20, v137, v141
	v_cvt_pk_bf16_f32 v21, v147, v149
	v_cvt_pk_bf16_f32 v22, v151, v153
	v_cvt_pk_bf16_f32 v23, v155, v157
	s_nop 0
	v_pk_fma_f32 v[128:129], v[130:131], v[218:219], v[56:57]
	v_cvt_pk_bf16_f32 v56, v104, v106
	v_cvt_pk_bf16_f32 v57, v112, v114
	v_cvt_pk_bf16_f32 v58, v132, v134
	v_cvt_pk_bf16_f32 v59, v138, v142
	v_cvt_pk_bf16_f32 v76, v136, v140
	v_cvt_pk_bf16_f32 v77, v146, v148
	v_cvt_pk_bf16_f32 v78, v150, v152
	v_cvt_pk_bf16_f32 v79, v154, v156
	ds_read_b64_tr_b16 v[82:83], v192 offset:29952
	ds_read_b64_tr_b16 v[80:81], v192 offset:27648
	ds_read_b64_tr_b16 v[84:85], v192 offset:27680
	ds_read_b64_tr_b16 v[86:87], v192 offset:29984
	s_waitcnt lgkmcnt(2)
	v_mfma_f32_16x16x32_bf16 v[72:75], v[80:83], v[60:63], v[72:75]
	v_mfma_f32_16x16x32_bf16 v[80:83], v[80:83], v[56:59], v[96:99]
	s_waitcnt lgkmcnt(0)
	v_mfma_f32_16x16x32_bf16 v[96:99], v[84:87], v[60:63], v[64:67]
	s_nop 2
	ds_read_b64_tr_b16 v[64:65], v192 offset:27712
	ds_read_b64_tr_b16 v[66:67], v192 offset:30016
	v_mfma_f32_16x16x32_bf16 v[84:87], v[84:87], v[56:59], v[92:95]
	s_waitcnt lgkmcnt(0)
	v_mfma_f32_16x16x32_bf16 v[92:95], v[64:67], v[60:63], v[52:55]
	s_nop 2
	ds_read_b64_tr_b16 v[52:53], v192 offset:27744
	ds_read_b64_tr_b16 v[54:55], v192 offset:30048
	v_mfma_f32_16x16x32_bf16 v[88:91], v[64:67], v[56:59], v[88:91]
	s_waitcnt lgkmcnt(0)
	v_mfma_f32_16x16x32_bf16 v[24:27], v[52:55], v[60:63], v[24:27]
	v_mfma_f32_16x16x32_bf16 v[68:71], v[52:55], v[56:59], v[68:71]
	ds_read_b64_tr_b16 v[54:55], v193 offset:29952
	ds_read_b64_tr_b16 v[52:53], v193 offset:27648
	ds_read_b64_tr_b16 v[56:57], v193 offset:27680
	ds_read_b64_tr_b16 v[58:59], v193 offset:29984
	ds_read_b64_tr_b16 v[60:61], v193 offset:27712
	ds_read_b64_tr_b16 v[62:63], v193 offset:30016
	s_waitcnt lgkmcnt(4)
	v_mfma_f32_16x16x32_bf16 v[64:67], v[52:55], v[20:23], v[72:75]
	s_waitcnt lgkmcnt(2)
	v_mfma_f32_16x16x32_bf16 v[72:75], v[56:59], v[20:23], v[96:99]
	v_mfma_f32_16x16x32_bf16 v[56:59], v[56:59], v[76:79], v[84:87]
	s_nop 2
	ds_read_b64_tr_b16 v[84:85], v193 offset:27744
	ds_read_b64_tr_b16 v[86:87], v193 offset:30048
	v_mfma_f32_16x16x32_bf16 v[52:55], v[52:55], v[76:79], v[80:83]
	s_waitcnt lgkmcnt(2)
	v_mfma_f32_16x16x32_bf16 v[80:83], v[60:63], v[20:23], v[92:95]
	v_mfma_f32_16x16x32_bf16 v[60:63], v[60:63], v[76:79], v[88:91]
	s_waitcnt lgkmcnt(0)
	v_mfma_f32_16x16x32_bf16 v[100:103], v[84:87], v[20:23], v[24:27]
	v_mfma_f32_16x16x32_bf16 v[84:87], v[84:87], v[76:79], v[68:71]

.LBB0_596:
	ds_read_b128 v[88:91], v191
	v_mov_b32_e32 v131, v129
	s_waitcnt lgkmcnt(0)
	v_mfma_f32_16x16x32_bf16 v[40:43], v[88:91], v[12:15], v[40:43]
	ds_read_b128 v[88:91], v191 offset:64
	s_waitcnt lgkmcnt(0)
	v_mfma_f32_16x16x32_bf16 v[40:43], v[88:91], v[16:19], v[40:43]
	ds_read_b128 v[88:91], v191 offset:2304
	s_waitcnt lgkmcnt(0)
	v_mfma_f32_16x16x32_bf16 v[36:39], v[88:91], v[12:15], v[36:39]
	ds_read_b128 v[88:91], v191 offset:2368
	s_waitcnt lgkmcnt(0)
	v_mfma_f32_16x16x32_bf16 v[36:39], v[88:91], v[16:19], v[36:39]
	ds_read_b128 v[88:91], v191 offset:4608
	s_waitcnt lgkmcnt(0)
	v_mfma_f32_16x16x32_bf16 v[76:79], v[88:91], v[12:15], v[76:79]
	ds_read_b128 v[88:91], v191 offset:4672
	s_waitcnt lgkmcnt(0)
	v_mfma_f32_16x16x32_bf16 v[76:79], v[88:91], v[16:19], v[76:79]
	ds_read_b128 v[88:91], v191 offset:6912
	s_nop 6
	s_waitcnt lgkmcnt(0)
	v_mfma_f32_16x16x32_bf16 v[68:71], v[88:91], v[12:15], v[68:71]
	ds_read_b128 v[88:91], v191 offset:6976
	s_waitcnt lgkmcnt(0)
	v_mfma_f32_16x16x32_bf16 v[68:71], v[88:91], v[16:19], v[68:71]
	v_max_f32_e32 v88, v42, v43
	v_max_f32_e32 v89, v38, v39
	v_max_f32_e32 v90, v76, v77
	v_max_f32_e32 v91, v78, v79
	s_nop 3
	v_max_f32_e32 v92, v70, v71
	v_max3_f32 v92, v68, v69, v92
	v_max3_f32 v88, v40, v41, v88
	v_max3_f32 v89, v36, v37, v89
	v_max3_f32 v90, v90, v91, v92
	v_max3_f32 v88, v88, v89, v90
	v_mov_b32_e32 v89, v88
	s_nop 1
	v_permlane32_swap_b32_e32 v88, v89
	v_max_f32_e32 v88, v88, v89
	v_mov_b32_e32 v89, v88
	s_nop 1
	v_permlane16_swap_b32_e32 v88, v89
	v_max3_f32 v219, v3, v88, v89
	v_sub_f32_e32 v41, v41, v219
	v_exp_f32_e32 v110, v41
	v_sub_f32_e32 v41, v42, v219
	v_sub_f32_e32 v42, v43, v219
	v_sub_f32_e32 v36, v36, v219
	v_exp_f32_e32 v111, v42
	v_exp_f32_e32 v42, v36
	v_sub_f32_e32 v36, v37, v219
	v_exp_f32_e32 v112, v36
	v_sub_f32_e32 v36, v38, v219
	v_exp_f32_e32 v43, v36
	v_sub_f32_e32 v36, v39, v219
	v_exp_f32_e32 v113, v36
	v_sub_f32_e32 v36, v76, v219
	v_exp_f32_e32 v76, v36
	v_sub_f32_e32 v36, v77, v219
	v_exp_f32_e32 v114, v36
	v_sub_f32_e32 v36, v78, v219
	v_exp_f32_e32 v77, v36
	v_sub_f32_e32 v36, v79, v219
	v_sub_f32_e32 v40, v40, v219
	v_exp_f32_e32 v115, v36
	v_sub_f32_e32 v36, v68, v219
	v_exp_f32_e32 v40, v40
	v_exp_f32_e32 v41, v41
	v_exp_f32_e32 v68, v36
	v_sub_f32_e32 v36, v69, v219
	v_exp_f32_e32 v78, v36
	v_sub_f32_e32 v36, v70, v219
	v_exp_f32_e32 v69, v36
	v_sub_f32_e32 v36, v71, v219
	v_exp_f32_e32 v79, v36
	v_pk_add_f32 v[36:37], v[42:43], v[40:41]
	v_pk_add_f32 v[38:39], v[112:113], v[110:111]
	v_pk_add_f32 v[36:37], v[76:77], v[36:37]
	v_pk_add_f32 v[38:39], v[114:115], v[38:39]
	v_pk_add_f32 v[36:37], v[68:69], v[36:37]
	v_pk_add_f32 v[38:39], v[78:79], v[38:39]
	v_sub_f32_e32 v88, v3, v219
	v_pk_add_f32 v[36:37], v[36:37], v[38:39]
	v_exp_f32_e32 v108, v88
	v_add_f32_e32 v130, v36, v37
	v_cvt_pk_bf16_f32 v36, v40, v110
	v_cvt_pk_bf16_f32 v37, v41, v111
	v_cvt_pk_bf16_f32 v38, v42, v112
	v_cvt_pk_bf16_f32 v39, v43, v113
	v_cvt_pk_bf16_f32 v40, v76, v114
	v_cvt_pk_bf16_f32 v41, v77, v115
	v_cvt_pk_bf16_f32 v42, v68, v78
	v_cvt_pk_bf16_f32 v43, v69, v79
	ds_read_b64_tr_b16 v[70:71], v192 offset:11520
	ds_read_b64_tr_b16 v[68:69], v192 offset:9216
	ds_read_b64_tr_b16 v[76:77], v192 offset:9248
	ds_read_b64_tr_b16 v[78:79], v192 offset:11552
	v_pk_mul_f32 v[90:91], v[54:55], v[108:109] op_sel_hi:[1,0]
	v_pk_mul_f32 v[88:89], v[52:53], v[108:109] op_sel_hi:[1,0]
	v_pk_mul_f32 v[94:95], v[58:59], v[108:109] op_sel_hi:[1,0]
	v_pk_mul_f32 v[92:93], v[56:57], v[108:109] op_sel_hi:[1,0]
	s_waitcnt lgkmcnt(2)
	v_mfma_f32_16x16x32_bf16 v[68:71], v[68:71], v[36:39], v[88:91]
	s_nop 2
	ds_read_b64_tr_b16 v[88:89], v192 offset:9280
	ds_read_b64_tr_b16 v[90:91], v192 offset:11584
	v_pk_mul_f32 v[98:99], v[62:63], v[108:109] op_sel_hi:[1,0]
	v_pk_mul_f32 v[96:97], v[60:61], v[108:109] op_sel_hi:[1,0]
	s_waitcnt lgkmcnt(2)
	v_mfma_f32_16x16x32_bf16 v[76:79], v[76:79], v[36:39], v[92:95]
	s_nop 2
	ds_read_b64_tr_b16 v[92:93], v192 offset:9312
	ds_read_b64_tr_b16 v[94:95], v192 offset:11616
	v_pk_mul_f32 v[106:107], v[86:87], v[108:109] op_sel_hi:[1,0]
	v_pk_mul_f32 v[104:105], v[84:85], v[108:109] op_sel_hi:[1,0]
	s_waitcnt lgkmcnt(2)
	v_mfma_f32_16x16x32_bf16 v[88:91], v[88:91], v[36:39], v[96:99]
	v_fmac_f32_e32 v130, v128, v108
	s_waitcnt lgkmcnt(0)
	v_mfma_f32_16x16x32_bf16 v[36:39], v[92:95], v[36:39], v[104:107]
	ds_read_b64_tr_b16 v[94:95], v193 offset:11520
	ds_read_b64_tr_b16 v[92:93], v193 offset:9216
	ds_read_b64_tr_b16 v[96:97], v193 offset:9248
	ds_read_b64_tr_b16 v[98:99], v193 offset:11552
	s_waitcnt lgkmcnt(2)
	v_mfma_f32_16x16x32_bf16 v[68:71], v[92:95], v[40:43], v[68:71]
	ds_read_b64_tr_b16 v[92:93], v193 offset:9280
	ds_read_b64_tr_b16 v[94:95], v193 offset:11584
	s_waitcnt lgkmcnt(0)
	v_mfma_f32_16x16x32_bf16 v[88:91], v[92:95], v[40:43], v[88:91]
	ds_read_b64_tr_b16 v[92:93], v193 offset:9312
	ds_read_b64_tr_b16 v[94:95], v193 offset:11616
	v_mfma_f32_16x16x32_bf16 v[76:79], v[96:99], v[40:43], v[76:79]
	s_waitcnt lgkmcnt(0)
	v_mfma_f32_16x16x32_bf16 v[108:111], v[92:95], v[40:43], v[36:39]

.LBB0_607:
	ds_read_b128 v[88:91], v191
	v_mov_b32_e32 v130, v128
	v_mov_b32_e32 v219, v3
	s_waitcnt lgkmcnt(0)
	v_mfma_f32_16x16x32_bf16 v[40:43], v[88:91], v[4:7], v[40:43]
	ds_read_b128 v[88:91], v191 offset:64
	s_waitcnt lgkmcnt(0)
	v_mfma_f32_16x16x32_bf16 v[40:43], v[88:91], v[8:11], v[40:43]
	ds_read_b128 v[88:91], v191 offset:2304
	s_waitcnt lgkmcnt(0)
	v_mfma_f32_16x16x32_bf16 v[36:39], v[88:91], v[4:7], v[36:39]
	ds_read_b128 v[88:91], v191 offset:2368
	s_waitcnt lgkmcnt(0)
	v_mfma_f32_16x16x32_bf16 v[36:39], v[88:91], v[8:11], v[36:39]
	ds_read_b128 v[88:91], v191 offset:4608
	s_waitcnt lgkmcnt(0)
	v_mfma_f32_16x16x32_bf16 v[76:79], v[88:91], v[4:7], v[76:79]
	ds_read_b128 v[88:91], v191 offset:4672
	s_waitcnt lgkmcnt(0)
	v_mfma_f32_16x16x32_bf16 v[76:79], v[88:91], v[8:11], v[76:79]
	ds_read_b128 v[88:91], v191 offset:6912
	s_nop 6
	s_waitcnt lgkmcnt(0)
	v_mfma_f32_16x16x32_bf16 v[68:71], v[88:91], v[4:7], v[68:71]
	ds_read_b128 v[88:91], v191 offset:6976
	s_waitcnt lgkmcnt(0)
	v_mfma_f32_16x16x32_bf16 v[68:71], v[88:91], v[8:11], v[68:71]
	v_max_f32_e32 v88, v42, v43
	v_max_f32_e32 v89, v38, v39
	v_max_f32_e32 v90, v76, v77
	v_max_f32_e32 v91, v78, v79
	s_nop 3
	v_max_f32_e32 v92, v70, v71
	v_max3_f32 v92, v68, v69, v92
	v_max3_f32 v88, v40, v41, v88
	v_max3_f32 v89, v36, v37, v89
	v_max3_f32 v90, v90, v91, v92
	v_max3_f32 v88, v88, v89, v90
	v_mov_b32_e32 v89, v88
	s_nop 1
	v_permlane32_swap_b32_e32 v88, v89
	v_max_f32_e32 v88, v88, v89
	v_mov_b32_e32 v89, v88
	s_nop 1
	v_permlane16_swap_b32_e32 v88, v89
	v_max3_f32 v220, v217, v88, v89
	v_sub_f32_e32 v41, v41, v220
	v_exp_f32_e32 v110, v41
	v_sub_f32_e32 v41, v42, v220
	v_sub_f32_e32 v42, v43, v220
	v_sub_f32_e32 v36, v36, v220
	v_exp_f32_e32 v111, v42
	v_exp_f32_e32 v42, v36
	v_sub_f32_e32 v36, v37, v220
	v_exp_f32_e32 v112, v36
	v_sub_f32_e32 v36, v38, v220
	v_exp_f32_e32 v43, v36
	v_sub_f32_e32 v36, v39, v220
	v_exp_f32_e32 v113, v36
	v_sub_f32_e32 v36, v76, v220
	v_exp_f32_e32 v76, v36
	v_sub_f32_e32 v36, v77, v220
	v_exp_f32_e32 v114, v36
	v_sub_f32_e32 v36, v78, v220
	v_exp_f32_e32 v77, v36
	v_sub_f32_e32 v36, v79, v220
	v_sub_f32_e32 v40, v40, v220
	v_exp_f32_e32 v115, v36
	v_sub_f32_e32 v36, v68, v220
	v_exp_f32_e32 v40, v40
	v_exp_f32_e32 v41, v41
	v_exp_f32_e32 v68, v36
	v_sub_f32_e32 v36, v69, v220
	v_exp_f32_e32 v78, v36
	v_sub_f32_e32 v36, v70, v220
	v_exp_f32_e32 v69, v36
	v_sub_f32_e32 v36, v71, v220
	v_exp_f32_e32 v79, v36
	v_pk_add_f32 v[36:37], v[42:43], v[40:41]
	v_pk_add_f32 v[38:39], v[112:113], v[110:111]
	v_pk_add_f32 v[36:37], v[76:77], v[36:37]
	v_pk_add_f32 v[38:39], v[114:115], v[38:39]
	v_pk_add_f32 v[36:37], v[68:69], v[36:37]
	v_pk_add_f32 v[38:39], v[78:79], v[38:39]
	v_sub_f32_e32 v88, v217, v220
	v_pk_add_f32 v[36:37], v[36:37], v[38:39]
	v_exp_f32_e32 v108, v88
	v_add_f32_e32 v131, v36, v37
	v_cvt_pk_bf16_f32 v36, v40, v110
	v_cvt_pk_bf16_f32 v37, v41, v111
	v_cvt_pk_bf16_f32 v38, v42, v112
	v_cvt_pk_bf16_f32 v39, v43, v113
	v_cvt_pk_bf16_f32 v40, v76, v114
	v_cvt_pk_bf16_f32 v41, v77, v115
	v_cvt_pk_bf16_f32 v42, v68, v78
	v_cvt_pk_bf16_f32 v43, v69, v79
	ds_read_b64_tr_b16 v[70:71], v192 offset:11520
	ds_read_b64_tr_b16 v[68:69], v192 offset:9216
	ds_read_b64_tr_b16 v[76:77], v192 offset:9248
	ds_read_b64_tr_b16 v[78:79], v192 offset:11552
	v_pk_mul_f32 v[90:91], v[66:67], v[108:109] op_sel_hi:[1,0]
	v_pk_mul_f32 v[88:89], v[64:65], v[108:109] op_sel_hi:[1,0]
	v_pk_mul_f32 v[94:95], v[74:75], v[108:109] op_sel_hi:[1,0]
	v_pk_mul_f32 v[92:93], v[72:73], v[108:109] op_sel_hi:[1,0]
	s_waitcnt lgkmcnt(2)
	v_mfma_f32_16x16x32_bf16 v[68:71], v[68:71], v[36:39], v[88:91]
	s_nop 2
	ds_read_b64_tr_b16 v[88:89], v192 offset:9280
	ds_read_b64_tr_b16 v[90:91], v192 offset:11584
	v_pk_mul_f32 v[98:99], v[82:83], v[108:109] op_sel_hi:[1,0]
	v_pk_mul_f32 v[96:97], v[80:81], v[108:109] op_sel_hi:[1,0]
	s_waitcnt lgkmcnt(2)
	v_mfma_f32_16x16x32_bf16 v[76:79], v[76:79], v[36:39], v[92:95]
	s_nop 2
	ds_read_b64_tr_b16 v[92:93], v192 offset:9312
	ds_read_b64_tr_b16 v[94:95], v192 offset:11616
	v_pk_mul_f32 v[106:107], v[102:103], v[108:109] op_sel_hi:[1,0]
	v_pk_mul_f32 v[104:105], v[100:101], v[108:109] op_sel_hi:[1,0]
	s_waitcnt lgkmcnt(2)
	v_mfma_f32_16x16x32_bf16 v[88:91], v[88:91], v[36:39], v[96:99]
	v_fmac_f32_e32 v131, v129, v108
	v_mov_b64_e32 v[110:111], v[86:87]
	v_mov_b64_e32 v[108:109], v[84:85]
	s_waitcnt lgkmcnt(0)
	v_mfma_f32_16x16x32_bf16 v[36:39], v[92:95], v[36:39], v[104:107]
	ds_read_b64_tr_b16 v[94:95], v193 offset:11520
	ds_read_b64_tr_b16 v[92:93], v193 offset:9216
	ds_read_b64_tr_b16 v[96:97], v193 offset:9248
	ds_read_b64_tr_b16 v[98:99], v193 offset:11552
	s_waitcnt lgkmcnt(2)
	v_mfma_f32_16x16x32_bf16 v[92:95], v[92:95], v[40:43], v[68:71]
	s_nop 2
	ds_read_b64_tr_b16 v[68:69], v193 offset:9280
	ds_read_b64_tr_b16 v[70:71], v193 offset:11584
	s_waitcnt lgkmcnt(0)
	v_mfma_f32_16x16x32_bf16 v[104:107], v[68:71], v[40:43], v[88:91]
	ds_read_b64_tr_b16 v[68:69], v193 offset:9312
	ds_read_b64_tr_b16 v[70:71], v193 offset:11616
	s_nop 0
	v_mov_b64_e32 v[90:91], v[62:63]
	v_mov_b64_e32 v[88:89], v[60:61]
	v_mfma_f32_16x16x32_bf16 v[96:99], v[96:99], v[40:43], v[76:79]
	s_waitcnt lgkmcnt(0)
	v_mfma_f32_16x16x32_bf16 v[112:115], v[68:71], v[40:43], v[36:39]
	v_mov_b64_e32 v[70:71], v[54:55]
	v_mov_b64_e32 v[78:79], v[58:59]
	v_mov_b64_e32 v[68:69], v[52:53]
	v_mov_b64_e32 v[76:77], v[56:57]

.LBB0_626:
	ds_read_b128 v[108:111], v191
	ds_read_b128 v[112:115], v191 offset:64
	s_waitcnt lgkmcnt(1)
	v_mfma_f32_16x16x32_bf16 v[68:71], v[108:111], v[4:7], v[68:71]
	v_mfma_f32_16x16x32_bf16 v[92:95], v[108:111], v[12:15], v[92:95]
	s_waitcnt lgkmcnt(0)
	v_mfma_f32_16x16x32_bf16 v[108:111], v[112:115], v[8:11], v[68:71]
	v_mfma_f32_16x16x32_bf16 v[68:71], v[112:115], v[16:19], v[92:95]
	s_nop 4
	ds_read_b128 v[92:95], v191 offset:2304
	s_waitcnt lgkmcnt(0)
	v_mfma_f32_16x16x32_bf16 v[36:39], v[92:95], v[4:7], v[36:39]
	v_mfma_f32_16x16x32_bf16 v[88:91], v[92:95], v[12:15], v[88:91]
	ds_read_b128 v[92:95], v191 offset:2368
	s_waitcnt lgkmcnt(0)
	v_mfma_f32_16x16x32_bf16 v[36:39], v[92:95], v[8:11], v[36:39]
	v_mfma_f32_16x16x32_bf16 v[92:95], v[92:95], v[16:19], v[88:91]
	s_nop 3
	ds_read_b128 v[88:91], v191 offset:4608
	s_waitcnt lgkmcnt(0)
	v_mfma_f32_16x16x32_bf16 v[76:79], v[88:91], v[4:7], v[76:79]
	v_mfma_f32_16x16x32_bf16 v[88:91], v[88:91], v[12:15], v[96:99]
	s_nop 2
	ds_read_b128 v[96:99], v191 offset:4672
	s_waitcnt lgkmcnt(0)
	v_mfma_f32_16x16x32_bf16 v[148:151], v[96:99], v[8:11], v[76:79]
	s_nop 2
	ds_read_b128 v[76:79], v191 offset:6912
	v_mfma_f32_16x16x32_bf16 v[96:99], v[96:99], v[16:19], v[88:91]
	s_nop 2
	ds_read_b128 v[88:91], v191 offset:6976
	s_waitcnt lgkmcnt(1)
	v_mfma_f32_16x16x32_bf16 v[40:43], v[76:79], v[4:7], v[40:43]
	v_mfma_f32_16x16x32_bf16 v[76:79], v[76:79], v[12:15], v[104:107]
	s_waitcnt lgkmcnt(0)
	v_mfma_f32_16x16x32_bf16 v[154:157], v[88:91], v[8:11], v[40:43]
	s_nop 4
	v_max_f32_e32 v40, v110, v111
	v_max_f32_e32 v41, v38, v39
	v_mfma_f32_16x16x32_bf16 v[104:107], v[88:91], v[16:19], v[76:79]
	v_max_f32_e32 v42, v148, v149
	v_max3_f32 v40, v108, v109, v40
	v_max_f32_e32 v43, v150, v151
	v_max_f32_e32 v76, v156, v157
	v_max3_f32 v76, v154, v155, v76
	v_max3_f32 v41, v36, v37, v41
	v_max3_f32 v42, v42, v43, v76
	v_max3_f32 v40, v40, v41, v42
	v_mov_b32_e32 v41, v40
	s_nop 1
	v_permlane32_swap_b32_e32 v40, v41
	v_max_f32_e32 v40, v40, v41
	v_mov_b32_e32 v41, v40
	s_nop 1
	v_permlane16_swap_b32_e32 v40, v41
	v_max3_f32 v220, v217, v40, v41
	v_sub_f32_e32 v40, v217, v220
	v_exp_f32_e32 v130, v40
	v_sub_f32_e32 v36, v36, v220
	v_exp_f32_e32 v133, v36
	v_sub_f32_e32 v36, v37, v220
	v_pk_mul_f32 v[88:89], v[64:65], v[130:131] op_sel_hi:[1,0]
	v_pk_mul_f32 v[64:65], v[80:81], v[130:131] op_sel_hi:[1,0]
	v_pk_mul_f32 v[90:91], v[66:67], v[130:131] op_sel_hi:[1,0]
	v_pk_mul_f32 v[66:67], v[82:83], v[130:131] op_sel_hi:[1,0]
	v_max_f32_e32 v80, v70, v71
	v_max_f32_e32 v81, v94, v95
	v_pk_mul_f32 v[40:41], v[100:101], v[130:131] op_sel_hi:[1,0]
	v_max_f32_e32 v82, v96, v97
	v_max_f32_e32 v83, v98, v99
	v_max_f32_e32 v100, v106, v107
	v_max3_f32 v100, v104, v105, v100
	v_max3_f32 v80, v68, v69, v80
	v_max3_f32 v81, v92, v93, v81
	v_max3_f32 v82, v82, v83, v100
	v_max3_f32 v80, v80, v81, v82
	v_mov_b32_e32 v81, v80
	s_nop 1
	v_permlane32_swap_b32_e32 v80, v81
	v_max_f32_e32 v80, v80, v81
	v_mov_b32_e32 v81, v80
	s_nop 1
	v_permlane16_swap_b32_e32 v80, v81
	v_max3_f32 v219, v3, v80, v81
	v_sub_f32_e32 v3, v3, v219
	v_exp_f32_e32 v222, v3
	v_sub_f32_e32 v3, v68, v219
	v_exp_f32_e32 v112, v3
	v_sub_f32_e32 v3, v69, v219
	v_pk_mul_f32 v[76:77], v[72:73], v[130:131] op_sel_hi:[1,0]
	v_sub_f32_e32 v72, v108, v220
	v_exp_f32_e32 v108, v3
	v_sub_f32_e32 v3, v70, v219
	v_exp_f32_e32 v113, v72
	v_sub_f32_e32 v72, v109, v220
	v_exp_f32_e32 v114, v3
	v_sub_f32_e32 v3, v71, v219
	v_exp_f32_e32 v109, v72
	v_sub_f32_e32 v72, v110, v220
	v_exp_f32_e32 v110, v3
	v_sub_f32_e32 v3, v92, v219
	v_exp_f32_e32 v132, v3
	v_sub_f32_e32 v3, v93, v219
	v_exp_f32_e32 v137, v36
	v_sub_f32_e32 v36, v38, v220
	v_exp_f32_e32 v136, v3
	v_sub_f32_e32 v3, v94, v219
	v_exp_f32_e32 v139, v36
	v_sub_f32_e32 v36, v39, v220
	v_exp_f32_e32 v138, v3
	v_sub_f32_e32 v3, v95, v219
	v_exp_f32_e32 v147, v36
	v_sub_f32_e32 v36, v148, v220
	v_exp_f32_e32 v146, v3
	v_sub_f32_e32 v3, v96, v219
	v_exp_f32_e32 v135, v36
	v_sub_f32_e32 v36, v149, v220
	v_exp_f32_e32 v134, v3
	v_sub_f32_e32 v3, v97, v219
	v_exp_f32_e32 v141, v36
	v_sub_f32_e32 v36, v150, v220
	v_exp_f32_e32 v140, v3
	v_sub_f32_e32 v3, v98, v219
	v_exp_f32_e32 v143, v36
	v_sub_f32_e32 v36, v151, v220
	v_exp_f32_e32 v142, v3
	v_sub_f32_e32 v3, v99, v219
	v_exp_f32_e32 v115, v72
	v_sub_f32_e32 v72, v111, v220
	v_exp_f32_e32 v149, v36
	v_sub_f32_e32 v36, v154, v220
	v_exp_f32_e32 v148, v3
	v_sub_f32_e32 v3, v104, v219
	v_exp_f32_e32 v111, v72
	v_exp_f32_e32 v151, v36
	v_sub_f32_e32 v36, v155, v220
	v_exp_f32_e32 v150, v3
	v_sub_f32_e32 v3, v105, v219
	v_exp_f32_e32 v153, v36
	v_sub_f32_e32 v36, v156, v220
	v_exp_f32_e32 v152, v3
	v_sub_f32_e32 v3, v106, v219
	v_exp_f32_e32 v155, v36
	v_sub_f32_e32 v36, v157, v220
	v_exp_f32_e32 v154, v3
	v_sub_f32_e32 v3, v107, v219
	v_exp_f32_e32 v157, v36
	v_exp_f32_e32 v156, v3
	v_pk_mul_f32 v[82:83], v[58:59], v[222:223] op_sel_hi:[1,0]
	v_pk_mul_f32 v[80:81], v[56:57], v[222:223] op_sel_hi:[1,0]
	v_pk_add_f32 v[56:57], v[132:133], v[112:113]
	v_pk_add_f32 v[58:59], v[136:137], v[108:109]
	v_pk_add_f32 v[68:69], v[138:139], v[114:115]
	v_pk_add_f32 v[70:71], v[146:147], v[110:111]
	v_pk_add_f32 v[56:57], v[134:135], v[56:57]
	v_pk_add_f32 v[58:59], v[140:141], v[58:59]
	v_pk_add_f32 v[68:69], v[142:143], v[68:69]
	v_pk_add_f32 v[70:71], v[148:149], v[70:71]
	v_pk_add_f32 v[56:57], v[150:151], v[56:57]
	v_pk_add_f32 v[58:59], v[152:153], v[58:59]
	v_pk_add_f32 v[68:69], v[154:155], v[68:69]
	v_pk_add_f32 v[70:71], v[156:157], v[70:71]
	v_pk_add_f32 v[56:57], v[56:57], v[58:59]
	v_pk_add_f32 v[58:59], v[68:69], v[70:71]
	v_pk_mul_f32 v[42:43], v[102:103], v[130:131] op_sel_hi:[1,0]
	v_pk_mul_f32 v[102:103], v[54:55], v[222:223] op_sel_hi:[1,0]
	v_pk_mul_f32 v[100:101], v[52:53], v[222:223] op_sel_hi:[1,0]
	v_pk_mul_f32 v[62:63], v[62:63], v[222:223] op_sel_hi:[1,0]
	v_pk_mul_f32 v[60:61], v[60:61], v[222:223] op_sel_hi:[1,0]
	v_pk_mul_f32 v[54:55], v[86:87], v[222:223] op_sel_hi:[1,0]
	v_pk_mul_f32 v[52:53], v[84:85], v[222:223] op_sel_hi:[1,0]
	v_mov_b32_e32 v223, v130
	v_pk_add_f32 v[56:57], v[56:57], v[58:59]
	v_pk_mul_f32 v[78:79], v[74:75], v[130:131] op_sel_hi:[1,0]
	v_cvt_pk_bf16_f32 v72, v113, v109
	v_cvt_pk_bf16_f32 v73, v115, v111
	v_cvt_pk_bf16_f32 v74, v133, v137
	v_cvt_pk_bf16_f32 v75, v139, v147
	v_cvt_pk_bf16_f32 v36, v135, v141
	v_cvt_pk_bf16_f32 v37, v143, v149
	v_cvt_pk_bf16_f32 v38, v151, v153
	v_cvt_pk_bf16_f32 v39, v155, v157
	v_pk_fma_f32 v[130:131], v[128:129], v[222:223], v[56:57]
	v_cvt_pk_bf16_f32 v68, v112, v108
	v_cvt_pk_bf16_f32 v69, v114, v110
	v_cvt_pk_bf16_f32 v70, v132, v136
	v_cvt_pk_bf16_f32 v71, v138, v146
	v_cvt_pk_bf16_f32 v56, v134, v140
	v_cvt_pk_bf16_f32 v57, v142, v148
	v_cvt_pk_bf16_f32 v58, v150, v152
	v_cvt_pk_bf16_f32 v59, v154, v156
	ds_read_b64_tr_b16 v[86:87], v192 offset:11520
	ds_read_b64_tr_b16 v[84:85], v192 offset:9216
	ds_read_b64_tr_b16 v[92:93], v192 offset:9248
	ds_read_b64_tr_b16 v[94:95], v192 offset:11552
	s_waitcnt lgkmcnt(0)
	v_mfma_f32_16x16x32_bf16 v[76:79], v[92:95], v[72:75], v[76:79]
	v_mfma_f32_16x16x32_bf16 v[80:83], v[92:95], v[68:71], v[80:83]
	ds_read_b64_tr_b16 v[92:93], v192 offset:9280
	ds_read_b64_tr_b16 v[94:95], v192 offset:11584
	s_waitcnt lgkmcnt(0)
	v_mfma_f32_16x16x32_bf16 v[64:67], v[92:95], v[72:75], v[64:67]
	v_mfma_f32_16x16x32_bf16 v[60:63], v[92:95], v[68:71], v[60:63]
	ds_read_b64_tr_b16 v[92:93], v192 offset:9312
	ds_read_b64_tr_b16 v[94:95], v192 offset:11616
	v_mfma_f32_16x16x32_bf16 v[88:91], v[84:87], v[72:75], v[88:91]
	v_mfma_f32_16x16x32_bf16 v[84:87], v[84:87], v[68:71], v[100:103]
	s_waitcnt lgkmcnt(0)
	v_mfma_f32_16x16x32_bf16 v[40:43], v[92:95], v[72:75], v[40:43]
	v_mfma_f32_16x16x32_bf16 v[52:55], v[92:95], v[68:71], v[52:55]
	ds_read_b64_tr_b16 v[70:71], v193 offset:11520
	ds_read_b64_tr_b16 v[68:69], v193 offset:9216
	ds_read_b64_tr_b16 v[72:73], v193 offset:9248
	ds_read_b64_tr_b16 v[74:75], v193 offset:11552
	s_waitcnt lgkmcnt(0)
	v_mfma_f32_16x16x32_bf16 v[96:99], v[72:75], v[36:39], v[76:79]
	v_mfma_f32_16x16x32_bf16 v[76:79], v[72:75], v[56:59], v[80:83]
	ds_read_b64_tr_b16 v[72:73], v193 offset:9280
	ds_read_b64_tr_b16 v[74:75], v193 offset:11584
	v_mfma_f32_16x16x32_bf16 v[92:95], v[68:71], v[36:39], v[88:91]
	s_waitcnt lgkmcnt(0)
	v_mfma_f32_16x16x32_bf16 v[88:91], v[72:75], v[56:59], v[60:63]
	s_nop 2
	ds_read_b64_tr_b16 v[60:61], v193 offset:9312
	ds_read_b64_tr_b16 v[62:63], v193 offset:11616
	v_mfma_f32_16x16x32_bf16 v[68:71], v[68:71], v[56:59], v[84:87]
	v_mfma_f32_16x16x32_bf16 v[104:107], v[72:75], v[36:39], v[64:67]
	s_waitcnt lgkmcnt(0)
	v_mfma_f32_16x16x32_bf16 v[112:115], v[60:63], v[36:39], v[40:43]
	v_mfma_f32_16x16x32_bf16 v[108:111], v[60:63], v[56:59], v[52:55]

; __device__ __forceinline__ float rows_max(float x) {
;     auto a = __builtin_amdgcn_permlane32_swap(__float_as_uint(x), __float_as_uint(x), false, false); x = fmaxf(__uint_as_float(a[0]), __uint_as_float(a[1]));
;     auto b = __builtin_amdgcn_permlane16_swap(__float_as_uint(x), __float_as_uint(x), false, false); return fmaxf(__uint_as_float(b[0]), __uint_as_float(b[1])); }
.LBB0_638:
	ds_read_b128 v[60:63], v191 offset:18432
	v_mov_b32_e32 v129, v131
	s_waitcnt lgkmcnt(0)
	v_mfma_f32_16x16x32_bf16 v[48:51], v[60:63], v[12:15], v[48:51]
	ds_read_b128 v[60:63], v191 offset:18496
	s_waitcnt lgkmcnt(0)
	v_mfma_f32_16x16x32_bf16 v[48:51], v[60:63], v[16:19], v[48:51]
	ds_read_b128 v[60:63], v191 offset:20736
	s_nop 6
	s_waitcnt lgkmcnt(0)
	v_mfma_f32_16x16x32_bf16 v[44:47], v[60:63], v[12:15], v[44:47]
	ds_read_b128 v[60:63], v191 offset:20800
	s_waitcnt lgkmcnt(0)
	v_mfma_f32_16x16x32_bf16 v[44:47], v[60:63], v[16:19], v[44:47]
	ds_read_b128 v[60:63], v191 offset:23040
	s_waitcnt lgkmcnt(0)
	v_mfma_f32_16x16x32_bf16 v[56:59], v[60:63], v[12:15], v[56:59]
	ds_read_b128 v[60:63], v191 offset:23104
	s_waitcnt lgkmcnt(0)
	v_mfma_f32_16x16x32_bf16 v[56:59], v[60:63], v[16:19], v[56:59]
	ds_read_b128 v[60:63], v191 offset:25344
	s_waitcnt lgkmcnt(0)
	v_mfma_f32_16x16x32_bf16 v[52:55], v[60:63], v[12:15], v[52:55]
	ds_read_b128 v[60:63], v191 offset:25408
	s_waitcnt lgkmcnt(0)
	v_mfma_f32_16x16x32_bf16 v[52:55], v[60:63], v[16:19], v[52:55]
	v_max_f32_e32 v3, v50, v51
	v_max_f32_e32 v60, v46, v47
	v_max_f32_e32 v61, v56, v57
	v_max_f32_e32 v62, v58, v59
	s_nop 3
	v_max_f32_e32 v63, v54, v55
	v_max3_f32 v63, v52, v53, v63
	v_max3_f32 v3, v48, v49, v3
	v_max3_f32 v60, v44, v45, v60
	v_max3_f32 v61, v61, v62, v63
	v_max3_f32 v3, v3, v60, v61
	v_mov_b32_e32 v60, v3
	s_nop 1
	v_permlane32_swap_b32_e32 v3, v60
	v_max_f32_e32 v3, v3, v60
	v_mov_b32_e32 v60, v3
	s_nop 1
	v_permlane16_swap_b32_e32 v3, v60
	v_max3_f32 v217, v219, v3, v60
	v_sub_f32_e32 v3, v219, v217
	v_exp_f32_e32 v84, v3
	v_sub_f32_e32 v3, v48, v217
	v_exp_f32_e32 v48, v3
	v_sub_f32_e32 v3, v49, v217
	v_exp_f32_e32 v86, v3
	v_sub_f32_e32 v3, v50, v217
	v_exp_f32_e32 v49, v3
	v_sub_f32_e32 v3, v51, v217
	v_exp_f32_e32 v87, v3
	v_sub_f32_e32 v3, v44, v217
	v_exp_f32_e32 v50, v3
	v_sub_f32_e32 v3, v45, v217
	v_exp_f32_e32 v100, v3
	v_sub_f32_e32 v3, v46, v217
	v_exp_f32_e32 v51, v3
	v_sub_f32_e32 v3, v47, v217
	v_exp_f32_e32 v101, v3
	v_sub_f32_e32 v3, v56, v217
	v_exp_f32_e32 v56, v3
	v_sub_f32_e32 v3, v57, v217
	v_exp_f32_e32 v102, v3
	v_sub_f32_e32 v3, v58, v217
	v_exp_f32_e32 v57, v3
	v_sub_f32_e32 v3, v59, v217
	v_exp_f32_e32 v103, v3
	v_sub_f32_e32 v3, v52, v217
	v_exp_f32_e32 v52, v3
	v_sub_f32_e32 v3, v53, v217
	v_exp_f32_e32 v58, v3
	v_sub_f32_e32 v3, v54, v217
	v_exp_f32_e32 v53, v3
	v_sub_f32_e32 v3, v55, v217
	v_exp_f32_e32 v59, v3
	v_pk_add_f32 v[44:45], v[50:51], v[48:49]
	v_pk_add_f32 v[46:47], v[100:101], v[86:87]
	v_pk_add_f32 v[44:45], v[56:57], v[44:45]
	v_pk_add_f32 v[46:47], v[102:103], v[46:47]
	v_pk_add_f32 v[44:45], v[52:53], v[44:45]
	v_pk_add_f32 v[46:47], v[58:59], v[46:47]
	v_pk_mul_f32 v[62:63], v[70:71], v[84:85] op_sel_hi:[1,0]
	v_pk_add_f32 v[44:45], v[44:45], v[46:47]
	v_pk_mul_f32 v[60:61], v[68:69], v[84:85] op_sel_hi:[1,0]
	v_add_f32_e32 v128, v44, v45
	v_cvt_pk_bf16_f32 v44, v48, v86
	v_cvt_pk_bf16_f32 v45, v49, v87
	v_cvt_pk_bf16_f32 v46, v50, v100
	v_cvt_pk_bf16_f32 v47, v51, v101
	v_cvt_pk_bf16_f32 v48, v56, v102
	v_cvt_pk_bf16_f32 v49, v57, v103
	v_cvt_pk_bf16_f32 v50, v52, v58
	v_cvt_pk_bf16_f32 v51, v53, v59
	ds_read_b64_tr_b16 v[54:55], v192 offset:29952
	ds_read_b64_tr_b16 v[52:53], v192 offset:27648
	ds_read_b64_tr_b16 v[56:57], v192 offset:27680
	ds_read_b64_tr_b16 v[58:59], v192 offset:29984
	v_pk_mul_f32 v[66:67], v[78:79], v[84:85] op_sel_hi:[1,0]
	v_pk_mul_f32 v[64:65], v[76:77], v[84:85] op_sel_hi:[1,0]
	s_waitcnt lgkmcnt(2)
	v_mfma_f32_16x16x32_bf16 v[52:55], v[52:55], v[44:47], v[60:63]
	s_nop 2
	ds_read_b64_tr_b16 v[60:61], v192 offset:27712
	ds_read_b64_tr_b16 v[62:63], v192 offset:30016
	v_pk_mul_f32 v[74:75], v[90:91], v[84:85] op_sel_hi:[1,0]
	v_pk_mul_f32 v[72:73], v[88:89], v[84:85] op_sel_hi:[1,0]
	s_waitcnt lgkmcnt(2)
	v_mfma_f32_16x16x32_bf16 v[56:59], v[56:59], v[44:47], v[64:67]
	s_nop 2
	ds_read_b64_tr_b16 v[64:65], v192 offset:27744
	ds_read_b64_tr_b16 v[66:67], v192 offset:30048
	v_pk_mul_f32 v[82:83], v[110:111], v[84:85] op_sel_hi:[1,0]
	v_pk_mul_f32 v[80:81], v[108:109], v[84:85] op_sel_hi:[1,0]
	s_waitcnt lgkmcnt(2)
	v_mfma_f32_16x16x32_bf16 v[60:63], v[60:63], v[44:47], v[72:75]
	v_fmac_f32_e32 v128, v130, v84
	s_waitcnt lgkmcnt(0)
	v_mfma_f32_16x16x32_bf16 v[44:47], v[64:67], v[44:47], v[80:83]
	ds_read_b64_tr_b16 v[66:67], v193 offset:29952
	ds_read_b64_tr_b16 v[64:65], v193 offset:27648
	ds_read_b64_tr_b16 v[72:73], v193 offset:27680
	ds_read_b64_tr_b16 v[74:75], v193 offset:29984
	s_waitcnt lgkmcnt(2)
	v_mfma_f32_16x16x32_bf16 v[52:55], v[64:67], v[48:51], v[52:55]
	ds_read_b64_tr_b16 v[64:65], v193 offset:27712
	ds_read_b64_tr_b16 v[66:67], v193 offset:30016
	s_waitcnt lgkmcnt(0)
	v_mfma_f32_16x16x32_bf16 v[60:63], v[64:67], v[48:51], v[60:63]
	ds_read_b64_tr_b16 v[64:65], v193 offset:27744
	ds_read_b64_tr_b16 v[66:67], v193 offset:30048
	v_mfma_f32_16x16x32_bf16 v[56:59], v[72:75], v[48:51], v[56:59]
	s_waitcnt lgkmcnt(0)
	v_mfma_f32_16x16x32_bf16 v[64:67], v[64:67], v[48:51], v[44:47]

; __device__ __forceinline__ float rows_max(float x) {
;     auto a = __builtin_amdgcn_permlane32_swap(__float_as_uint(x), __float_as_uint(x), false, false); x = fmaxf(__uint_as_float(a[0]), __uint_as_float(a[1]));
;     auto b = __builtin_amdgcn_permlane16_swap(__float_as_uint(x), __float_as_uint(x), false, false); return fmaxf(__uint_as_float(b[0]), __uint_as_float(b[1])); }
.LBB0_649:
	ds_read_b128 v[60:63], v191 offset:18432
	v_mov_b32_e32 v128, v130
	v_mov_b32_e32 v217, v219
	s_waitcnt lgkmcnt(0)
	v_mfma_f32_16x16x32_bf16 v[48:51], v[60:63], v[4:7], v[48:51]
	ds_read_b128 v[60:63], v191 offset:18496
	s_waitcnt lgkmcnt(0)
	v_mfma_f32_16x16x32_bf16 v[48:51], v[60:63], v[8:11], v[48:51]
	ds_read_b128 v[60:63], v191 offset:20736
	s_nop 6
	s_waitcnt lgkmcnt(0)
	v_mfma_f32_16x16x32_bf16 v[44:47], v[60:63], v[4:7], v[44:47]
	ds_read_b128 v[60:63], v191 offset:20800
	s_waitcnt lgkmcnt(0)
	v_mfma_f32_16x16x32_bf16 v[44:47], v[60:63], v[8:11], v[44:47]
	ds_read_b128 v[60:63], v191 offset:23040
	s_waitcnt lgkmcnt(0)
	v_mfma_f32_16x16x32_bf16 v[56:59], v[60:63], v[4:7], v[56:59]
	ds_read_b128 v[60:63], v191 offset:23104
	s_waitcnt lgkmcnt(0)
	v_mfma_f32_16x16x32_bf16 v[56:59], v[60:63], v[8:11], v[56:59]
	ds_read_b128 v[60:63], v191 offset:25344
	s_waitcnt lgkmcnt(0)
	v_mfma_f32_16x16x32_bf16 v[52:55], v[60:63], v[4:7], v[52:55]
	ds_read_b128 v[60:63], v191 offset:25408
	s_waitcnt lgkmcnt(0)
	v_mfma_f32_16x16x32_bf16 v[52:55], v[60:63], v[8:11], v[52:55]
	v_max_f32_e32 v3, v50, v51
	v_max_f32_e32 v60, v46, v47
	v_max_f32_e32 v61, v56, v57
	v_max_f32_e32 v62, v58, v59
	s_nop 3
	v_max_f32_e32 v63, v54, v55
	v_max3_f32 v63, v52, v53, v63
	v_max3_f32 v3, v48, v49, v3
	v_max3_f32 v60, v44, v45, v60
	v_max3_f32 v61, v61, v62, v63
	v_max3_f32 v3, v3, v60, v61
	v_mov_b32_e32 v60, v3
	s_nop 1
	v_permlane32_swap_b32_e32 v3, v60
	v_max_f32_e32 v3, v3, v60
	v_mov_b32_e32 v60, v3
	s_nop 1
	v_permlane16_swap_b32_e32 v3, v60
	v_max3_f32 v218, v220, v3, v60
	v_sub_f32_e32 v3, v220, v218
	v_exp_f32_e32 v84, v3
	v_sub_f32_e32 v3, v48, v218
	v_exp_f32_e32 v48, v3
	v_sub_f32_e32 v3, v49, v218
	v_exp_f32_e32 v86, v3
	v_sub_f32_e32 v3, v50, v218
	v_exp_f32_e32 v49, v3
	v_sub_f32_e32 v3, v51, v218
	v_exp_f32_e32 v87, v3
	v_sub_f32_e32 v3, v44, v218
	v_exp_f32_e32 v50, v3
	v_sub_f32_e32 v3, v45, v218
	v_exp_f32_e32 v100, v3
	v_sub_f32_e32 v3, v46, v218
	v_exp_f32_e32 v51, v3
	v_sub_f32_e32 v3, v47, v218
	v_exp_f32_e32 v101, v3
	v_sub_f32_e32 v3, v56, v218
	v_exp_f32_e32 v56, v3
	v_sub_f32_e32 v3, v57, v218
	v_exp_f32_e32 v102, v3
	v_sub_f32_e32 v3, v58, v218
	v_exp_f32_e32 v57, v3
	v_sub_f32_e32 v3, v59, v218
	v_exp_f32_e32 v103, v3
	v_sub_f32_e32 v3, v52, v218
	v_exp_f32_e32 v52, v3
	v_sub_f32_e32 v3, v53, v218
	v_exp_f32_e32 v58, v3
	v_sub_f32_e32 v3, v54, v218
	v_exp_f32_e32 v53, v3
	v_sub_f32_e32 v3, v55, v218
	v_exp_f32_e32 v59, v3
	v_pk_add_f32 v[44:45], v[50:51], v[48:49]
	v_pk_add_f32 v[46:47], v[100:101], v[86:87]
	v_pk_add_f32 v[44:45], v[56:57], v[44:45]
	v_pk_add_f32 v[46:47], v[102:103], v[46:47]
	v_pk_add_f32 v[44:45], v[52:53], v[44:45]
	v_pk_add_f32 v[46:47], v[58:59], v[46:47]
	v_pk_mul_f32 v[62:63], v[94:95], v[84:85] op_sel_hi:[1,0]
	v_pk_add_f32 v[44:45], v[44:45], v[46:47]
	v_pk_mul_f32 v[60:61], v[92:93], v[84:85] op_sel_hi:[1,0]
	v_add_f32_e32 v129, v44, v45
	v_cvt_pk_bf16_f32 v44, v48, v86
	v_cvt_pk_bf16_f32 v45, v49, v87
	v_cvt_pk_bf16_f32 v46, v50, v100
	v_cvt_pk_bf16_f32 v47, v51, v101
	v_cvt_pk_bf16_f32 v48, v56, v102
	v_cvt_pk_bf16_f32 v49, v57, v103
	v_cvt_pk_bf16_f32 v50, v52, v58
	v_cvt_pk_bf16_f32 v51, v53, v59
	ds_read_b64_tr_b16 v[54:55], v192 offset:29952
	ds_read_b64_tr_b16 v[52:53], v192 offset:27648
	ds_read_b64_tr_b16 v[56:57], v192 offset:27680
	ds_read_b64_tr_b16 v[58:59], v192 offset:29984
	v_pk_mul_f32 v[66:67], v[98:99], v[84:85] op_sel_hi:[1,0]
	v_pk_mul_f32 v[64:65], v[96:97], v[84:85] op_sel_hi:[1,0]
	s_waitcnt lgkmcnt(2)
	v_mfma_f32_16x16x32_bf16 v[52:55], v[52:55], v[44:47], v[60:63]
	s_nop 2
	ds_read_b64_tr_b16 v[60:61], v192 offset:27712
	ds_read_b64_tr_b16 v[62:63], v192 offset:30016
	v_pk_mul_f32 v[74:75], v[106:107], v[84:85] op_sel_hi:[1,0]
	v_pk_mul_f32 v[72:73], v[104:105], v[84:85] op_sel_hi:[1,0]
	s_waitcnt lgkmcnt(2)
	v_mfma_f32_16x16x32_bf16 v[56:59], v[56:59], v[44:47], v[64:67]
	s_nop 2
	ds_read_b64_tr_b16 v[64:65], v192 offset:27744
	ds_read_b64_tr_b16 v[66:67], v192 offset:30048
	v_pk_mul_f32 v[82:83], v[114:115], v[84:85] op_sel_hi:[1,0]
	v_pk_mul_f32 v[80:81], v[112:113], v[84:85] op_sel_hi:[1,0]
	s_waitcnt lgkmcnt(2)
	v_mfma_f32_16x16x32_bf16 v[60:63], v[60:63], v[44:47], v[72:75]
	v_fmac_f32_e32 v129, v131, v84
	s_waitcnt lgkmcnt(0)
	v_mfma_f32_16x16x32_bf16 v[44:47], v[64:67], v[44:47], v[80:83]
	ds_read_b64_tr_b16 v[66:67], v193 offset:29952
	ds_read_b64_tr_b16 v[64:65], v193 offset:27648
	s_nop 0
	ds_read_b64_tr_b16 v[80:81], v193 offset:27680
	ds_read_b64_tr_b16 v[82:83], v193 offset:29984
	s_waitcnt lgkmcnt(2)
	v_mfma_f32_16x16x32_bf16 v[72:75], v[64:67], v[48:51], v[52:55]
	s_nop 2
	ds_read_b64_tr_b16 v[52:53], v193 offset:27712
	ds_read_b64_tr_b16 v[54:55], v193 offset:30016
	v_mov_b64_e32 v[64:65], v[108:109]
	v_mov_b64_e32 v[66:67], v[110:111]
	s_waitcnt lgkmcnt(0)
	v_mfma_f32_16x16x32_bf16 v[84:87], v[52:55], v[48:51], v[60:63]
	ds_read_b64_tr_b16 v[52:53], v193 offset:27744
	ds_read_b64_tr_b16 v[54:55], v193 offset:30048
	s_nop 0
	v_mov_b64_e32 v[60:61], v[88:89]
	v_mov_b64_e32 v[62:63], v[90:91]
	v_mfma_f32_16x16x32_bf16 v[80:83], v[80:83], v[48:51], v[56:59]
	s_waitcnt lgkmcnt(0)
	v_mfma_f32_16x16x32_bf16 v[100:103], v[52:55], v[48:51], v[44:47]
	v_mov_b64_e32 v[52:53], v[68:69]
	v_mov_b64_e32 v[56:57], v[76:77]
	v_mov_b64_e32 v[54:55], v[70:71]
	v_mov_b64_e32 v[58:59], v[78:79]
